# attention unit output stores nt (on top of P1 + conversion nt)
# baseline (speedup 1.0000x reference)
.LBB0_473:
	s_or_b64 exec, exec, s[18:19]
	s_waitcnt lgkmcnt(0)
	ds_read_b128 v[60:63], v228 offset:128
	ds_read_b128 v[64:67], v228 offset:160
	s_or_b32 s2, s20, 32
	s_waitcnt lgkmcnt(1)
	v_rcp_f32_e32 v1, v60
	v_cmp_lt_f32_e32 vcc, 0, v60
	v_rcp_f32_e32 v68, v61
	s_nop 0
	v_cndmask_b32_e32 v1, 0, v1, vcc
	v_mul_f32_e32 v34, v34, v1
	v_mul_f32_e32 v1, v18, v1
	v_bfe_u32 v18, v34, 16, 1
	v_bfe_u32 v60, v1, 16, 1
	v_add3_u32 v18, v34, v18, s48
	v_add3_u32 v1, v1, v60, s48
	v_cmp_lt_f32_e32 vcc, 0, v61
	ds_write_b16_d16_hi v5, v18
	ds_write_b16_d16_hi v5, v1 offset:64
	v_cndmask_b32_e32 v1, 0, v68, vcc
	v_mul_f32_e32 v5, v35, v1
	v_bfe_u32 v18, v5, 16, 1
	v_add3_u32 v5, v5, v18, s48
	v_rcp_f32_e32 v18, v62
	v_mul_f32_e32 v1, v19, v1
	ds_write_b16_d16_hi v6, v5
	v_bfe_u32 v5, v1, 16, 1
	v_add3_u32 v1, v1, v5, s48
	v_cmp_lt_f32_e32 vcc, 0, v62
	ds_write_b16_d16_hi v6, v1 offset:64
	s_nop 0
	v_cndmask_b32_e32 v1, 0, v18, vcc
	v_mul_f32_e32 v5, v36, v1
	v_bfe_u32 v6, v5, 16, 1
	v_add3_u32 v5, v5, v6, s48
	v_rcp_f32_e32 v6, v63
	v_mul_f32_e32 v1, v20, v1
	ds_write_b16_d16_hi v7, v5
	v_bfe_u32 v5, v1, 16, 1
	v_add3_u32 v1, v1, v5, s48
	v_cmp_lt_f32_e32 vcc, 0, v63
	ds_write_b16_d16_hi v7, v1 offset:64
	s_nop 0
	v_cndmask_b32_e32 v1, 0, v6, vcc
	v_mul_f32_e32 v5, v37, v1
	v_bfe_u32 v6, v5, 16, 1
	v_add3_u32 v5, v5, v6, s48
	s_waitcnt lgkmcnt(6)
	v_rcp_f32_e32 v6, v64
	v_mul_f32_e32 v1, v21, v1
	ds_write_b16_d16_hi v8, v5
	v_bfe_u32 v5, v1, 16, 1
	v_add3_u32 v1, v1, v5, s48
	v_cmp_lt_f32_e32 vcc, 0, v64
	ds_write_b16_d16_hi v8, v1 offset:64
	ds_read_b128 v[18:21], v228 offset:224
	v_cndmask_b32_e32 v1, 0, v6, vcc
	v_mul_f32_e32 v5, v38, v1
	v_bfe_u32 v6, v5, 16, 1
	v_add3_u32 v5, v5, v6, s48
	v_rcp_f32_e32 v6, v65
	v_mul_f32_e32 v1, v22, v1
	ds_write_b16_d16_hi v9, v5
	v_bfe_u32 v5, v1, 16, 1
	v_add3_u32 v1, v1, v5, s48
	v_cmp_lt_f32_e32 vcc, 0, v65
	ds_write_b16_d16_hi v9, v1 offset:64
	s_nop 0
	v_cndmask_b32_e32 v1, 0, v6, vcc
	v_mul_f32_e32 v5, v39, v1
	v_bfe_u32 v6, v5, 16, 1
	v_add3_u32 v5, v5, v6, s48
	v_rcp_f32_e32 v6, v66
	v_mul_f32_e32 v1, v23, v1
	ds_write_b16_d16_hi v11, v5
	v_bfe_u32 v5, v1, 16, 1
	v_add3_u32 v1, v1, v5, s48
	v_cmp_lt_f32_e32 vcc, 0, v66
	ds_write_b16_d16_hi v11, v1 offset:64
	s_nop 0
	v_cndmask_b32_e32 v1, 0, v6, vcc
	v_mul_f32_e32 v5, v40, v1
	v_bfe_u32 v6, v5, 16, 1
	v_add3_u32 v5, v5, v6, s48
	v_rcp_f32_e32 v6, v67
	v_mul_f32_e32 v1, v24, v1
	ds_write_b16_d16_hi v12, v5
	v_bfe_u32 v5, v1, 16, 1
	v_add3_u32 v1, v1, v5, s48
	v_cmp_lt_f32_e32 vcc, 0, v67
	ds_write_b16_d16_hi v12, v1 offset:64
	s_nop 0
	v_cndmask_b32_e32 v1, 0, v6, vcc
	v_mul_f32_e32 v5, v41, v1
	v_bfe_u32 v6, v5, 16, 1
	v_add3_u32 v5, v5, v6, s48
	ds_read_b128 v[6:9], v228 offset:192
	v_mul_f32_e32 v1, v25, v1
	ds_write_b16_d16_hi v10, v5
	v_bfe_u32 v5, v1, 16, 1
	v_add3_u32 v1, v1, v5, s48
	s_waitcnt lgkmcnt(1)
	v_rcp_f32_e32 v11, v6
	v_cmp_lt_f32_e32 vcc, 0, v6
	ds_write_b16_d16_hi v10, v1 offset:64
	s_nop 0
	v_cndmask_b32_e32 v1, 0, v11, vcc
	v_mul_f32_e32 v5, v42, v1
	v_bfe_u32 v6, v5, 16, 1
	v_add3_u32 v5, v5, v6, s48
	v_rcp_f32_e32 v6, v7
	v_mul_f32_e32 v1, v26, v1
	ds_write_b16_d16_hi v13, v5
	v_bfe_u32 v5, v1, 16, 1
	v_add3_u32 v1, v1, v5, s48
	v_cmp_lt_f32_e32 vcc, 0, v7
	ds_write_b16_d16_hi v13, v1 offset:64
	s_nop 0
	v_cndmask_b32_e32 v1, 0, v6, vcc
	v_mul_f32_e32 v5, v43, v1
	v_bfe_u32 v6, v5, 16, 1
	v_add3_u32 v5, v5, v6, s48
	v_rcp_f32_e32 v6, v8
	v_mul_f32_e32 v1, v27, v1
	ds_write_b16_d16_hi v14, v5
	v_bfe_u32 v5, v1, 16, 1
	v_add3_u32 v1, v1, v5, s48
	v_cmp_lt_f32_e32 vcc, 0, v8
	ds_write_b16_d16_hi v14, v1 offset:64
	v_or_b32_e32 v8, s2, v4
	v_cndmask_b32_e32 v1, 0, v6, vcc
	v_mul_f32_e32 v5, v44, v1
	v_bfe_u32 v6, v5, 16, 1
	v_add3_u32 v5, v5, v6, s48
	v_rcp_f32_e32 v6, v9
	v_mul_f32_e32 v1, v28, v1
	ds_write_b16_d16_hi v15, v5
	v_bfe_u32 v5, v1, 16, 1
	v_add3_u32 v1, v1, v5, s48
	v_cmp_lt_f32_e32 vcc, 0, v9
	ds_write_b16_d16_hi v15, v1 offset:64
	v_mov_b32_e32 v9, s6
	v_cndmask_b32_e32 v1, 0, v6, vcc
	v_mul_f32_e32 v5, v45, v1
	v_bfe_u32 v6, v5, 16, 1
	v_add3_u32 v5, v5, v6, s48
	v_rcp_f32_e32 v6, v18
	v_mul_f32_e32 v1, v29, v1
	ds_write_b16_d16_hi v16, v5
	v_bfe_u32 v5, v1, 16, 1
	v_add3_u32 v1, v1, v5, s48
	v_cmp_lt_f32_e32 vcc, 0, v18
	ds_write_b16_d16_hi v16, v1 offset:64
	v_lshlrev_b64 v[8:9], 11, v[8:9]
	v_cndmask_b32_e32 v1, 0, v6, vcc
	v_mul_f32_e32 v5, v46, v1
	v_bfe_u32 v6, v5, 16, 1
	v_add3_u32 v5, v5, v6, s48
	v_rcp_f32_e32 v6, v19
	v_mul_f32_e32 v1, v30, v1
	ds_write_b16_d16_hi v17, v5
	v_bfe_u32 v5, v1, 16, 1
	v_add3_u32 v1, v1, v5, s48
	v_cmp_lt_f32_e32 vcc, 0, v19
	ds_write_b16_d16_hi v17, v1 offset:64
	v_lshl_add_u64 v[8:9], s[92:93], 0, v[8:9]
	v_cndmask_b32_e32 v1, 0, v6, vcc
	v_mul_f32_e32 v5, v47, v1
	v_bfe_u32 v6, v5, 16, 1
	v_add3_u32 v5, v5, v6, s48
	v_rcp_f32_e32 v6, v20
	v_mul_f32_e32 v1, v31, v1
	ds_write_b16_d16_hi v50, v5
	v_bfe_u32 v5, v1, 16, 1
	v_add3_u32 v1, v1, v5, s48
	v_cmp_lt_f32_e32 vcc, 0, v20
	ds_write_b16_d16_hi v50, v1 offset:64
	v_lshl_add_u64 v[8:9], v[8:9], 0, s[4:5]
	v_cndmask_b32_e32 v1, 0, v6, vcc
	v_mul_f32_e32 v5, v48, v1
	v_bfe_u32 v6, v5, 16, 1
	v_add3_u32 v5, v5, v6, s48
	v_rcp_f32_e32 v6, v21
	v_mul_f32_e32 v1, v32, v1
	ds_write_b16_d16_hi v51, v5
	v_bfe_u32 v5, v1, 16, 1
	v_add3_u32 v1, v1, v5, s48
	v_cmp_lt_f32_e32 vcc, 0, v21
	ds_write_b16_d16_hi v51, v1 offset:64
	v_lshl_add_u64 v[8:9], v[8:9], 0, v[2:3]
	v_cndmask_b32_e32 v1, 0, v6, vcc
	v_mul_f32_e32 v5, v49, v1
	v_bfe_u32 v6, v5, 16, 1
	v_add3_u32 v5, v5, v6, s48
	v_mul_f32_e32 v1, v33, v1
	ds_write_b16_d16_hi v52, v5
	v_bfe_u32 v5, v1, 16, 1
	v_add3_u32 v1, v1, v5, s48
	ds_write_b16_d16_hi v52, v1 offset:64
	s_waitcnt lgkmcnt(0)
	ds_read_b128 v[4:7], v54
	v_add_co_u32_e32 v12, vcc, s49, v8
	s_nop 1
	v_addc_co_u32_e32 v13, vcc, 0, v9, vcc
	ds_read_b128 v[8:11], v57
	s_waitcnt lgkmcnt(1)
	global_store_dwordx4 v[12:13], v[4:7], off offset:1024 nt
	s_nop 1
	v_mov_b32_e32 v5, s6
	v_or_b32_e32 v4, s2, v53
	v_lshlrev_b64 v[4:5], 11, v[4:5]
	v_lshl_add_u64 v[4:5], s[92:93], 0, v[4:5]
	v_lshl_add_u64 v[4:5], v[4:5], 0, s[4:5]
	v_lshl_add_u64 v[4:5], v[4:5], 0, v[2:3]
	v_add_co_u32_e32 v4, vcc, s49, v4
	s_nop 1
	v_addc_co_u32_e32 v5, vcc, 0, v5, vcc
	s_waitcnt lgkmcnt(0)
	global_store_dwordx4 v[4:5], v[8:11], off offset:1024 nt
	ds_read_b128 v[4:7], v58
	s_nop 0
	v_mov_b32_e32 v9, s6
	v_or_b32_e32 v8, s2, v56
	v_lshlrev_b64 v[8:9], 11, v[8:9]
	v_lshl_add_u64 v[8:9], s[92:93], 0, v[8:9]
	v_lshl_add_u64 v[8:9], v[8:9], 0, s[4:5]
	v_lshl_add_u64 v[8:9], v[8:9], 0, v[2:3]
	v_add_co_u32_e32 v12, vcc, s49, v8
	s_nop 1
	v_addc_co_u32_e32 v13, vcc, 0, v9, vcc
	ds_read_b128 v[8:11], v59
	s_waitcnt lgkmcnt(1)
	global_store_dwordx4 v[12:13], v[4:7], off offset:1024 nt
	s_nop 1
	v_mov_b32_e32 v5, s6
	v_or_b32_e32 v4, s2, v55
	v_lshlrev_b64 v[4:5], 11, v[4:5]
	v_lshl_add_u64 v[4:5], s[92:93], 0, v[4:5]
	v_lshl_add_u64 v[4:5], v[4:5], 0, s[4:5]
	v_lshl_add_u64 v[4:5], v[4:5], 0, v[2:3]
	v_add_co_u32_e32 v4, vcc, 0x33000000, v4
	s_mov_b64 s[2:3], 0
	s_nop 0
	v_addc_co_u32_e32 v5, vcc, 0, v5, vcc
	s_waitcnt lgkmcnt(0)
	global_store_dwordx4 v[4:5], v[8:11], off offset:1024 nt
	s_waitcnt lgkmcnt(0)

.LBB0_508:
	v_readlane_b32 s56, v255, 23
	v_mov_b32_e32 v2, v204
	v_readlane_b32 s57, v255, 24
	v_readlane_b32 s58, v255, 25
	v_cmp_gt_u32_e64 s[2:3], 32, v235
	v_permlane32_swap_b32_e32 v204, v2
	v_readlane_b32 s59, v255, 26
	s_and_saveexec_b64 s[4:5], s[2:3]
	v_add_f32_e32 v2, v204, v2
	ds_write_b32 v231, v2 offset:128
	s_or_b64 exec, exec, s[4:5]
	s_waitcnt lgkmcnt(0)
	ds_read_b128 v[6:9], v228 offset:128
	ds_read_b128 v[10:13], v228 offset:160
	s_lshl_b64 s[4:5], s[20:21], 11
	s_lshl_b32 s20, s50, 12
	s_add_i32 s20, s20, 0
	s_waitcnt lgkmcnt(1)
	v_rcp_f32_e32 v5, v6
	v_cmp_lt_f32_e32 vcc, 0, v6
	s_add_i32 s21, s20, 0x10c00
	v_rcp_f32_e32 v15, v7
	v_cndmask_b32_e32 v6, 0, v5, vcc
	v_mul_f32_e32 v5, v66, v6
	v_bfe_u32 v14, v5, 16, 1
	v_lshl_add_u32 v82, v230, 1, s21
	v_add3_u32 v14, v5, v14, s48
	v_lshlrev_b32_e32 v5, 9, v229
	v_add_u32_e32 v5, v82, v5
	v_mul_f32_e32 v6, v50, v6
	ds_write_b16_d16_hi v5, v14
	v_bfe_u32 v14, v6, 16, 1
	v_cmp_lt_f32_e32 vcc, 0, v7
	v_add3_u32 v6, v6, v14, s48
	ds_write_b16_d16_hi v5, v6 offset:64
	v_cndmask_b32_e32 v7, 0, v15, vcc
	v_mul_f32_e32 v6, v67, v7
	v_bfe_u32 v14, v6, 16, 1
	v_lshlrev_b32_e32 v66, 7, v237
	v_rcp_f32_e32 v15, v8
	v_add3_u32 v14, v6, v14, s48
	v_or_b32_e32 v6, 0x80, v66
	v_add_u32_e32 v6, v82, v6
	v_mul_f32_e32 v7, v51, v7
	ds_write_b16_d16_hi v6, v14
	v_bfe_u32 v14, v7, 16, 1
	v_cmp_lt_f32_e32 vcc, 0, v8
	v_add3_u32 v7, v7, v14, s48
	ds_write_b16_d16_hi v6, v7 offset:64
	v_cndmask_b32_e32 v8, 0, v15, vcc
	v_mul_f32_e32 v7, v68, v8
	v_bfe_u32 v14, v7, 16, 1
	v_rcp_f32_e32 v15, v9
	v_add3_u32 v14, v7, v14, s48
	v_or_b32_e32 v7, 0x100, v66
	v_add_u32_e32 v7, v82, v7
	v_mul_f32_e32 v8, v52, v8
	ds_write_b16_d16_hi v7, v14
	v_bfe_u32 v14, v8, 16, 1
	v_cmp_lt_f32_e32 vcc, 0, v9
	v_add3_u32 v8, v8, v14, s48
	ds_write_b16_d16_hi v7, v8 offset:64
	v_cndmask_b32_e32 v9, 0, v15, vcc
	v_mul_f32_e32 v8, v69, v9
	v_bfe_u32 v14, v8, 16, 1
	s_waitcnt lgkmcnt(6)
	v_rcp_f32_e32 v15, v10
	v_add3_u32 v14, v8, v14, s48
	v_or_b32_e32 v8, 0x180, v66
	v_add_u32_e32 v8, v82, v8
	v_mul_f32_e32 v9, v53, v9
	ds_write_b16_d16_hi v8, v14
	v_bfe_u32 v14, v9, 16, 1
	v_cmp_lt_f32_e32 vcc, 0, v10
	v_add3_u32 v9, v9, v14, s48
	ds_write_b16_d16_hi v8, v9 offset:64
	v_cndmask_b32_e32 v10, 0, v15, vcc
	v_mul_f32_e32 v9, v70, v10
	v_bfe_u32 v14, v9, 16, 1
	v_add3_u32 v14, v9, v14, s48
	v_or_b32_e32 v9, 0x400, v66
	v_rcp_f32_e32 v15, v11
	v_add_u32_e32 v9, v82, v9
	v_mul_f32_e32 v10, v54, v10
	ds_write_b16_d16_hi v9, v14
	v_bfe_u32 v14, v10, 16, 1
	v_add3_u32 v10, v10, v14, s48
	v_cmp_lt_f32_e32 vcc, 0, v11
	ds_write_b16_d16_hi v9, v10 offset:64
	s_add_u32 s20, s4, s6
	v_cndmask_b32_e32 v10, 0, v15, vcc
	v_mul_f32_e32 v11, v71, v10
	v_bfe_u32 v14, v11, 16, 1
	v_add3_u32 v14, v11, v14, s48
	v_or_b32_e32 v11, 0x480, v66
	v_rcp_f32_e32 v15, v12
	v_add_u32_e32 v11, v82, v11
	v_mul_f32_e32 v10, v55, v10
	ds_write_b16_d16_hi v11, v14
	v_bfe_u32 v14, v10, 16, 1
	v_add3_u32 v10, v10, v14, s48
	v_cmp_lt_f32_e32 vcc, 0, v12
	ds_write_b16_d16_hi v11, v10 offset:64
	v_and_b32_e32 v2, 56, v236
	v_cndmask_b32_e32 v10, 0, v15, vcc
	v_mul_f32_e32 v12, v72, v10
	v_bfe_u32 v14, v12, 16, 1
	v_rcp_f32_e32 v15, v13
	v_add3_u32 v14, v12, v14, s48
	v_or_b32_e32 v12, 0x500, v66
	v_add_u32_e32 v12, v82, v12
	v_mul_f32_e32 v10, v56, v10
	ds_write_b16_d16_hi v12, v14
	v_bfe_u32 v14, v10, 16, 1
	v_cmp_lt_f32_e32 vcc, 0, v13
	v_add3_u32 v10, v10, v14, s48
	ds_write_b16_d16_hi v12, v10 offset:64
	v_cndmask_b32_e32 v13, 0, v15, vcc
	v_mul_f32_e32 v10, v73, v13
	v_bfe_u32 v14, v10, 16, 1
	v_add3_u32 v50, v10, v14, s48
	ds_read_b128 v[14:17], v228 offset:192
	v_or_b32_e32 v10, 0x580, v66
	v_add_u32_e32 v10, v82, v10
	ds_write_b16_d16_hi v10, v50
	ds_read_b128 v[50:53], v228 offset:224
	s_waitcnt lgkmcnt(2)
	v_rcp_f32_e32 v55, v14
	v_mul_f32_e32 v13, v57, v13
	v_bfe_u32 v54, v13, 16, 1
	v_cmp_lt_f32_e32 vcc, 0, v14
	v_add3_u32 v13, v13, v54, s48
	ds_write_b16_d16_hi v10, v13 offset:64
	v_cndmask_b32_e32 v14, 0, v55, vcc
	v_mul_f32_e32 v13, v74, v14
	v_bfe_u32 v54, v13, 16, 1
	v_rcp_f32_e32 v55, v15
	v_add3_u32 v54, v13, v54, s48
	v_or_b32_e32 v13, 0x800, v66
	v_add_u32_e32 v13, v82, v13
	v_mul_f32_e32 v14, v58, v14
	ds_write_b16_d16_hi v13, v54
	v_bfe_u32 v54, v14, 16, 1
	v_cmp_lt_f32_e32 vcc, 0, v15
	v_add3_u32 v14, v14, v54, s48
	ds_write_b16_d16_hi v13, v14 offset:64
	v_cndmask_b32_e32 v15, 0, v55, vcc
	v_mul_f32_e32 v14, v75, v15
	v_bfe_u32 v54, v14, 16, 1
	v_rcp_f32_e32 v55, v16
	v_add3_u32 v54, v14, v54, s48
	v_or_b32_e32 v14, 0x880, v66
	v_add_u32_e32 v14, v82, v14
	v_mul_f32_e32 v15, v59, v15
	ds_write_b16_d16_hi v14, v54
	v_bfe_u32 v54, v15, 16, 1
	v_cmp_lt_f32_e32 vcc, 0, v16
	v_add3_u32 v15, v15, v54, s48
	ds_write_b16_d16_hi v14, v15 offset:64
	v_cndmask_b32_e32 v16, 0, v55, vcc
	v_mul_f32_e32 v15, v76, v16
	v_bfe_u32 v54, v15, 16, 1
	v_rcp_f32_e32 v55, v17
	v_add3_u32 v54, v15, v54, s48
	v_or_b32_e32 v15, 0x900, v66
	v_add_u32_e32 v15, v82, v15
	v_mul_f32_e32 v16, v60, v16
	ds_write_b16_d16_hi v15, v54
	v_bfe_u32 v54, v16, 16, 1
	v_cmp_lt_f32_e32 vcc, 0, v17
	v_add3_u32 v16, v16, v54, s48
	ds_write_b16_d16_hi v15, v16 offset:64
	v_cndmask_b32_e32 v17, 0, v55, vcc
	v_mul_f32_e32 v16, v77, v17
	v_bfe_u32 v54, v16, 16, 1
	s_waitcnt lgkmcnt(7)
	v_rcp_f32_e32 v55, v50
	v_add3_u32 v54, v16, v54, s48
	v_or_b32_e32 v16, 0x980, v66
	v_add_u32_e32 v16, v82, v16
	v_mul_f32_e32 v17, v61, v17
	ds_write_b16_d16_hi v16, v54
	v_bfe_u32 v54, v17, 16, 1
	v_cmp_lt_f32_e32 vcc, 0, v50
	v_add3_u32 v17, v17, v54, s48
	ds_write_b16_d16_hi v16, v17 offset:64
	v_cndmask_b32_e32 v50, 0, v55, vcc
	v_mul_f32_e32 v17, v78, v50
	v_bfe_u32 v54, v17, 16, 1
	v_rcp_f32_e32 v55, v51
	v_add3_u32 v54, v17, v54, s48
	v_or_b32_e32 v17, 0xc00, v66
	v_add_u32_e32 v17, v82, v17
	v_mul_f32_e32 v50, v62, v50
	ds_write_b16_d16_hi v17, v54
	v_bfe_u32 v54, v50, 16, 1
	v_cmp_lt_f32_e32 vcc, 0, v51
	v_add3_u32 v50, v50, v54, s48
	ds_write_b16_d16_hi v17, v50 offset:64
	v_cndmask_b32_e32 v51, 0, v55, vcc
	v_mul_f32_e32 v50, v79, v51
	v_bfe_u32 v54, v50, 16, 1
	v_rcp_f32_e32 v55, v52
	v_add3_u32 v54, v50, v54, s48
	v_or_b32_e32 v50, 0xc80, v66
	v_add_u32_e32 v50, v82, v50
	v_mul_f32_e32 v51, v63, v51
	ds_write_b16_d16_hi v50, v54
	v_bfe_u32 v54, v51, 16, 1
	v_cmp_lt_f32_e32 vcc, 0, v52
	v_add3_u32 v51, v51, v54, s48
	ds_write_b16_d16_hi v50, v51 offset:64
	v_cndmask_b32_e32 v52, 0, v55, vcc
	v_mul_f32_e32 v51, v80, v52
	v_bfe_u32 v54, v51, 16, 1
	v_rcp_f32_e32 v55, v53
	v_add3_u32 v54, v51, v54, s48
	v_or_b32_e32 v51, 0xd00, v66
	v_add_u32_e32 v51, v82, v51
	v_mul_f32_e32 v52, v64, v52
	ds_write_b16_d16_hi v51, v54
	v_bfe_u32 v54, v52, 16, 1
	v_cmp_lt_f32_e32 vcc, 0, v53
	v_add3_u32 v52, v52, v54, s48
	ds_write_b16_d16_hi v51, v52 offset:64
	v_cndmask_b32_e32 v53, 0, v55, vcc
	v_mul_f32_e32 v52, v81, v53
	v_bfe_u32 v54, v52, 16, 1
	v_add3_u32 v54, v52, v54, s48
	v_or_b32_e32 v52, 0xd80, v66
	v_add_u32_e32 v52, v82, v52
	v_mul_f32_e32 v53, v65, v53
	ds_write_b16_d16_hi v52, v54
	v_bfe_u32 v54, v53, 16, 1
	v_lshrrev_b32_e32 v4, 3, v235
	s_addc_u32 s6, s5, 0
	v_lshlrev_b32_e32 v2, 1, v2
	v_add3_u32 v53, v53, v54, s48
	v_add_u32_e32 v83, s21, v2
	ds_write_b16_d16_hi v52, v53 offset:64
	v_or_b32_e32 v68, s20, v4
	v_mov_b32_e32 v69, s6
	v_lshlrev_b32_e32 v53, 7, v4
	s_waitcnt lgkmcnt(0)
	v_add_u32_e32 v54, v83, v53
	v_lshlrev_b64 v[56:57], 11, v[68:69]
	ds_read_b128 v[58:61], v54
	v_lshl_add_u64 v[56:57], s[92:93], 0, v[56:57]
	s_lshl_b64 s[4:5], s[18:19], 1
	v_lshl_add_u64 v[56:57], v[56:57], 0, s[4:5]
	v_lshl_add_u64 v[56:57], v[56:57], 0, v[2:3]
	v_or_b32_e32 v53, 8, v4
	v_add_co_u32_e32 v66, vcc, s49, v56
	v_lshlrev_b32_e32 v55, 7, v53
	s_nop 0
	v_addc_co_u32_e32 v67, vcc, 0, v57, vcc
	v_add_u32_e32 v57, v83, v55
	v_or_b32_e32 v68, s20, v53
	ds_read_b128 v[62:65], v57
	s_waitcnt lgkmcnt(1)
	global_store_dwordx4 v[66:67], v[58:61], off offset:1024 nt
	v_or_b32_e32 v56, 16, v4
	v_lshlrev_b32_e32 v55, 7, v56
	v_lshlrev_b64 v[58:59], 11, v[68:69]
	v_lshl_add_u64 v[58:59], s[92:93], 0, v[58:59]
	v_lshl_add_u64 v[58:59], v[58:59], 0, s[4:5]
	v_lshl_add_u64 v[58:59], v[58:59], 0, v[2:3]
	v_add_co_u32_e32 v58, vcc, s49, v58
	v_or_b32_e32 v68, s20, v56
	s_nop 0
	v_addc_co_u32_e32 v59, vcc, 0, v59, vcc
	s_waitcnt lgkmcnt(0)
	global_store_dwordx4 v[58:59], v[62:65], off offset:1024 nt
	v_add_u32_e32 v58, v83, v55
	ds_read_b128 v[60:63], v58
	v_lshlrev_b64 v[64:65], 11, v[68:69]
	v_lshl_add_u64 v[64:65], s[92:93], 0, v[64:65]
	v_lshl_add_u64 v[64:65], v[64:65], 0, s[4:5]
	v_lshl_add_u64 v[64:65], v[64:65], 0, v[2:3]
	v_or_b32_e32 v55, 24, v4
	v_add_co_u32_e32 v70, vcc, s49, v64
	v_lshlrev_b32_e32 v59, 7, v55
	s_nop 0
	v_addc_co_u32_e32 v71, vcc, 0, v65, vcc
	v_add_u32_e32 v59, v83, v59
	v_or_b32_e32 v68, s20, v55
	ds_read_b128 v[64:67], v59
	s_waitcnt lgkmcnt(1)
	global_store_dwordx4 v[70:71], v[60:63], off offset:1024 nt
	s_nop 1
	v_lshlrev_b64 v[60:61], 11, v[68:69]
	v_lshl_add_u64 v[60:61], s[92:93], 0, v[60:61]
	v_lshl_add_u64 v[60:61], v[60:61], 0, s[4:5]
	v_lshl_add_u64 v[60:61], v[60:61], 0, v[2:3]
	v_add_co_u32_e32 v60, vcc, 0x33000000, v60
	s_nop 1
	v_addc_co_u32_e32 v61, vcc, 0, v61, vcc
	s_waitcnt lgkmcnt(0)
	global_store_dwordx4 v[60:61], v[64:67], off offset:1024 nt
	s_waitcnt lgkmcnt(0)
	v_mov_b32_e32 v60, v1
	s_nop 1
	v_permlane32_swap_b32_e32 v1, v60
	s_and_saveexec_b64 s[18:19], s[2:3]
	s_cbranch_execz .LBB0_473
	v_add_f32_e32 v1, v1, v60
	ds_write_b32 v231, v1 offset:128
	s_branch .LBB0_473

.LBB0_513:
	s_or_b64 exec, exec, s[10:11]
	s_waitcnt lgkmcnt(0)
	ds_read_b128 v[60:63], v199 offset:128
	ds_read_b128 v[64:67], v199 offset:160
	s_or_b32 s2, s12, 32
	s_waitcnt lgkmcnt(1)
	v_rcp_f32_e32 v68, v60
	v_cmp_lt_f32_e32 vcc, 0, v60
	v_rcp_f32_e32 v69, v61
	s_nop 0
	v_cndmask_b32_e32 v60, 0, v68, vcc
	v_mul_f32_e32 v34, v34, v60
	v_mul_f32_e32 v18, v18, v60
	v_bfe_u32 v60, v34, 16, 1
	v_bfe_u32 v68, v18, 16, 1
	v_add3_u32 v34, v34, v60, s27
	v_cmp_lt_f32_e32 vcc, 0, v61
	v_add3_u32 v18, v18, v68, s27
	ds_write_b16_d16_hi v5, v34
	ds_write_b16_d16_hi v5, v18 offset:64
	v_cndmask_b32_e32 v5, 0, v69, vcc
	v_mul_f32_e32 v18, v35, v5
	v_bfe_u32 v34, v18, 16, 1
	v_mul_f32_e32 v5, v19, v5
	v_rcp_f32_e32 v19, v62
	v_add3_u32 v18, v18, v34, s27
	ds_write_b16_d16_hi v6, v18
	v_bfe_u32 v18, v5, 16, 1
	v_add3_u32 v5, v5, v18, s27
	v_cmp_lt_f32_e32 vcc, 0, v62
	ds_write_b16_d16_hi v6, v5 offset:64
	s_nop 0
	v_cndmask_b32_e32 v5, 0, v19, vcc
	v_mul_f32_e32 v6, v36, v5
	v_bfe_u32 v18, v6, 16, 1
	v_add3_u32 v6, v6, v18, s27
	v_rcp_f32_e32 v18, v63
	v_mul_f32_e32 v5, v20, v5
	ds_write_b16_d16_hi v7, v6
	v_bfe_u32 v6, v5, 16, 1
	v_add3_u32 v5, v5, v6, s27
	v_cmp_lt_f32_e32 vcc, 0, v63
	ds_write_b16_d16_hi v7, v5 offset:64
	s_nop 0
	v_cndmask_b32_e32 v5, 0, v18, vcc
	v_mul_f32_e32 v6, v37, v5
	v_bfe_u32 v7, v6, 16, 1
	v_add3_u32 v6, v6, v7, s27
	s_waitcnt lgkmcnt(6)
	v_rcp_f32_e32 v7, v64
	v_mul_f32_e32 v5, v21, v5
	ds_write_b16_d16_hi v8, v6
	v_bfe_u32 v6, v5, 16, 1
	v_add3_u32 v5, v5, v6, s27
	v_cmp_lt_f32_e32 vcc, 0, v64
	ds_write_b16_d16_hi v8, v5 offset:64
	ds_read_b128 v[18:21], v199 offset:224
	v_cndmask_b32_e32 v5, 0, v7, vcc
	v_mul_f32_e32 v6, v38, v5
	v_bfe_u32 v7, v6, 16, 1
	v_add3_u32 v6, v6, v7, s27
	v_rcp_f32_e32 v7, v65
	v_mul_f32_e32 v5, v22, v5
	ds_write_b16_d16_hi v9, v6
	v_bfe_u32 v6, v5, 16, 1
	v_add3_u32 v5, v5, v6, s27
	v_cmp_lt_f32_e32 vcc, 0, v65
	ds_write_b16_d16_hi v9, v5 offset:64
	s_nop 0
	v_cndmask_b32_e32 v5, 0, v7, vcc
	v_mul_f32_e32 v6, v39, v5
	v_bfe_u32 v7, v6, 16, 1
	v_add3_u32 v6, v6, v7, s27
	v_rcp_f32_e32 v7, v66
	v_mul_f32_e32 v5, v23, v5
	ds_write_b16_d16_hi v11, v6
	v_bfe_u32 v6, v5, 16, 1
	v_add3_u32 v5, v5, v6, s27
	v_cmp_lt_f32_e32 vcc, 0, v66
	ds_write_b16_d16_hi v11, v5 offset:64
	s_nop 0
	v_cndmask_b32_e32 v5, 0, v7, vcc
	v_mul_f32_e32 v6, v40, v5
	v_bfe_u32 v7, v6, 16, 1
	v_add3_u32 v6, v6, v7, s27
	v_rcp_f32_e32 v7, v67
	v_mul_f32_e32 v5, v24, v5
	ds_write_b16_d16_hi v12, v6
	v_bfe_u32 v6, v5, 16, 1
	v_add3_u32 v5, v5, v6, s27
	v_cmp_lt_f32_e32 vcc, 0, v67
	ds_write_b16_d16_hi v12, v5 offset:64
	s_nop 0
	v_cndmask_b32_e32 v5, 0, v7, vcc
	v_mul_f32_e32 v6, v41, v5
	v_bfe_u32 v7, v6, 16, 1
	v_add3_u32 v11, v6, v7, s27
	ds_read_b128 v[6:9], v199 offset:192
	v_mul_f32_e32 v5, v25, v5
	ds_write_b16_d16_hi v10, v11
	v_bfe_u32 v11, v5, 16, 1
	v_add3_u32 v5, v5, v11, s27
	s_waitcnt lgkmcnt(1)
	v_rcp_f32_e32 v12, v6
	v_cmp_lt_f32_e32 vcc, 0, v6
	ds_write_b16_d16_hi v10, v5 offset:64
	s_nop 0
	v_cndmask_b32_e32 v5, 0, v12, vcc
	v_mul_f32_e32 v6, v42, v5
	v_bfe_u32 v10, v6, 16, 1
	v_add3_u32 v6, v6, v10, s27
	v_rcp_f32_e32 v10, v7
	v_mul_f32_e32 v5, v26, v5
	ds_write_b16_d16_hi v13, v6
	v_bfe_u32 v6, v5, 16, 1
	v_add3_u32 v5, v5, v6, s27
	v_cmp_lt_f32_e32 vcc, 0, v7
	ds_write_b16_d16_hi v13, v5 offset:64
	s_nop 0
	v_cndmask_b32_e32 v5, 0, v10, vcc
	v_mul_f32_e32 v6, v43, v5
	v_bfe_u32 v7, v6, 16, 1
	v_add3_u32 v6, v6, v7, s27
	v_rcp_f32_e32 v7, v8
	v_mul_f32_e32 v5, v27, v5
	ds_write_b16_d16_hi v14, v6
	v_bfe_u32 v6, v5, 16, 1
	v_add3_u32 v5, v5, v6, s27
	v_cmp_lt_f32_e32 vcc, 0, v8
	ds_write_b16_d16_hi v14, v5 offset:64
	v_or_b32_e32 v8, s2, v4
	v_cndmask_b32_e32 v5, 0, v7, vcc
	v_mul_f32_e32 v6, v44, v5
	v_bfe_u32 v7, v6, 16, 1
	v_add3_u32 v6, v6, v7, s27
	v_rcp_f32_e32 v7, v9
	v_mul_f32_e32 v5, v28, v5
	ds_write_b16_d16_hi v15, v6
	v_bfe_u32 v6, v5, 16, 1
	v_add3_u32 v5, v5, v6, s27
	v_cmp_lt_f32_e32 vcc, 0, v9
	ds_write_b16_d16_hi v15, v5 offset:64
	v_mov_b32_e32 v9, s6
	v_cndmask_b32_e32 v5, 0, v7, vcc
	v_mul_f32_e32 v6, v45, v5
	v_bfe_u32 v7, v6, 16, 1
	v_add3_u32 v6, v6, v7, s27
	v_rcp_f32_e32 v7, v18
	v_mul_f32_e32 v5, v29, v5
	ds_write_b16_d16_hi v16, v6
	v_bfe_u32 v6, v5, 16, 1
	v_add3_u32 v5, v5, v6, s27
	v_cmp_lt_f32_e32 vcc, 0, v18
	ds_write_b16_d16_hi v16, v5 offset:64
	v_lshlrev_b64 v[8:9], 10, v[8:9]
	v_cndmask_b32_e32 v5, 0, v7, vcc
	v_mul_f32_e32 v6, v46, v5
	v_bfe_u32 v7, v6, 16, 1
	v_add3_u32 v6, v6, v7, s27
	v_rcp_f32_e32 v7, v19
	v_mul_f32_e32 v5, v30, v5
	ds_write_b16_d16_hi v17, v6
	v_bfe_u32 v6, v5, 16, 1
	v_add3_u32 v5, v5, v6, s27
	v_cmp_lt_f32_e32 vcc, 0, v19
	ds_write_b16_d16_hi v17, v5 offset:64
	v_lshl_add_u64 v[8:9], s[4:5], 0, v[8:9]
	v_cndmask_b32_e32 v5, 0, v7, vcc
	v_mul_f32_e32 v6, v47, v5
	v_bfe_u32 v7, v6, 16, 1
	v_add3_u32 v6, v6, v7, s27
	v_rcp_f32_e32 v7, v20
	v_mul_f32_e32 v5, v31, v5
	ds_write_b16_d16_hi v50, v6
	v_bfe_u32 v6, v5, 16, 1
	v_add3_u32 v5, v5, v6, s27
	v_cmp_lt_f32_e32 vcc, 0, v20
	ds_write_b16_d16_hi v50, v5 offset:64
	v_lshl_add_u64 v[8:9], v[8:9], 0, s[8:9]
	v_cndmask_b32_e32 v5, 0, v7, vcc
	v_mul_f32_e32 v6, v48, v5
	v_bfe_u32 v7, v6, 16, 1
	v_add3_u32 v6, v6, v7, s27
	v_rcp_f32_e32 v7, v21
	v_mul_f32_e32 v5, v32, v5
	ds_write_b16_d16_hi v51, v6
	v_bfe_u32 v6, v5, 16, 1
	v_add3_u32 v5, v5, v6, s27
	v_cmp_lt_f32_e32 vcc, 0, v21
	ds_write_b16_d16_hi v51, v5 offset:64
	v_lshl_add_u64 v[12:13], v[8:9], 0, v[2:3]
	v_cndmask_b32_e32 v5, 0, v7, vcc
	v_mul_f32_e32 v6, v49, v5
	v_bfe_u32 v7, v6, 16, 1
	v_add3_u32 v6, v6, v7, s27
	v_mul_f32_e32 v5, v33, v5
	ds_write_b16_d16_hi v52, v6
	v_bfe_u32 v6, v5, 16, 1
	v_add3_u32 v5, v5, v6, s27
	ds_write_b16_d16_hi v52, v5 offset:64
	s_waitcnt lgkmcnt(0)
	ds_read_b128 v[4:7], v55
	ds_read_b128 v[8:11], v57
	s_waitcnt lgkmcnt(1)
	global_store_dwordx4 v[12:13], v[4:7], off nt
	s_nop 1
	v_mov_b32_e32 v5, s6
	v_or_b32_e32 v4, s2, v53
	v_lshlrev_b64 v[4:5], 10, v[4:5]
	v_lshl_add_u64 v[4:5], s[4:5], 0, v[4:5]
	v_lshl_add_u64 v[4:5], v[4:5], 0, s[8:9]
	v_lshl_add_u64 v[4:5], v[4:5], 0, v[2:3]
	s_waitcnt lgkmcnt(0)
	global_store_dwordx4 v[4:5], v[8:11], off nt
	ds_read_b128 v[4:7], v58
	s_nop 0
	v_mov_b32_e32 v9, s6
	v_or_b32_e32 v8, s2, v56
	v_lshlrev_b64 v[8:9], 10, v[8:9]
	v_lshl_add_u64 v[8:9], s[4:5], 0, v[8:9]
	v_lshl_add_u64 v[8:9], v[8:9], 0, s[8:9]
	v_lshl_add_u64 v[12:13], v[8:9], 0, v[2:3]
	ds_read_b128 v[8:11], v59
	s_waitcnt lgkmcnt(1)
	global_store_dwordx4 v[12:13], v[4:7], off nt
	s_nop 1
	v_mov_b32_e32 v5, s6
	v_or_b32_e32 v4, s2, v54
	v_lshlrev_b64 v[4:5], 10, v[4:5]
	v_lshl_add_u64 v[4:5], s[4:5], 0, v[4:5]
	v_lshl_add_u64 v[4:5], v[4:5], 0, s[8:9]
	v_lshl_add_u64 v[4:5], v[4:5], 0, v[2:3]
	s_waitcnt lgkmcnt(0)
	global_store_dwordx4 v[4:5], v[8:11], off nt
	s_waitcnt lgkmcnt(0)
	s_mov_b64 s[2:3], 0

.LBB0_542:
	v_mov_b32_e32 v2, v210
	s_nop 1
	v_permlane32_swap_b32_e32 v210, v2
	s_and_saveexec_b64 s[12:13], s[2:3]
	v_add_f32_e32 v2, v210, v2
	ds_write_b32 v200, v2 offset:128
	s_or_b64 exec, exec, s[12:13]
	s_waitcnt lgkmcnt(0)
	ds_read_b128 v[6:9], v199 offset:128
	ds_read_b128 v[10:13], v199 offset:160
	s_lshl_b32 s6, s31, 12
	s_add_i32 s6, s6, 0
	s_add_i32 s13, s6, 0x10c00
	s_waitcnt lgkmcnt(1)
	v_rcp_f32_e32 v5, v6
	v_cmp_lt_f32_e32 vcc, 0, v6
	v_rcp_f32_e32 v15, v7
	v_lshl_add_u32 v82, v203, 1, s13
	v_cndmask_b32_e32 v6, 0, v5, vcc
	v_mul_f32_e32 v5, v66, v6
	v_bfe_u32 v14, v5, 16, 1
	v_add3_u32 v14, v5, v14, s27
	v_lshlrev_b32_e32 v5, 9, v202
	v_add_u32_e32 v5, v82, v5
	v_mul_f32_e32 v6, v50, v6
	ds_write_b16_d16_hi v5, v14
	v_bfe_u32 v14, v6, 16, 1
	v_cmp_lt_f32_e32 vcc, 0, v7
	v_add3_u32 v6, v6, v14, s27
	ds_write_b16_d16_hi v5, v6 offset:64
	v_cndmask_b32_e32 v7, 0, v15, vcc
	v_mul_f32_e32 v6, v67, v7
	v_bfe_u32 v14, v6, 16, 1
	v_lshlrev_b32_e32 v66, 7, v206
	v_rcp_f32_e32 v15, v8
	v_add3_u32 v14, v6, v14, s27
	v_or_b32_e32 v6, 0x80, v66
	v_add_u32_e32 v6, v82, v6
	v_mul_f32_e32 v7, v51, v7
	ds_write_b16_d16_hi v6, v14
	v_bfe_u32 v14, v7, 16, 1
	v_cmp_lt_f32_e32 vcc, 0, v8
	v_add3_u32 v7, v7, v14, s27
	ds_write_b16_d16_hi v6, v7 offset:64
	v_cndmask_b32_e32 v8, 0, v15, vcc
	v_mul_f32_e32 v7, v68, v8
	v_bfe_u32 v14, v7, 16, 1
	v_rcp_f32_e32 v15, v9
	v_add3_u32 v14, v7, v14, s27
	v_or_b32_e32 v7, 0x100, v66
	v_add_u32_e32 v7, v82, v7
	v_mul_f32_e32 v8, v52, v8
	ds_write_b16_d16_hi v7, v14
	v_bfe_u32 v14, v8, 16, 1
	v_cmp_lt_f32_e32 vcc, 0, v9
	v_add3_u32 v8, v8, v14, s27
	ds_write_b16_d16_hi v7, v8 offset:64
	v_cndmask_b32_e32 v9, 0, v15, vcc
	v_mul_f32_e32 v8, v69, v9
	v_bfe_u32 v14, v8, 16, 1
	s_waitcnt lgkmcnt(6)
	v_rcp_f32_e32 v15, v10
	v_add3_u32 v14, v8, v14, s27
	v_or_b32_e32 v8, 0x180, v66
	v_add_u32_e32 v8, v82, v8
	v_mul_f32_e32 v9, v53, v9
	ds_write_b16_d16_hi v8, v14
	v_bfe_u32 v14, v9, 16, 1
	v_cmp_lt_f32_e32 vcc, 0, v10
	v_add3_u32 v9, v9, v14, s27
	ds_write_b16_d16_hi v8, v9 offset:64
	v_cndmask_b32_e32 v10, 0, v15, vcc
	v_mul_f32_e32 v9, v70, v10
	v_bfe_u32 v14, v9, 16, 1
	v_add3_u32 v14, v9, v14, s27
	v_or_b32_e32 v9, 0x400, v66
	v_rcp_f32_e32 v15, v11
	v_add_u32_e32 v9, v82, v9
	v_mul_f32_e32 v10, v54, v10
	ds_write_b16_d16_hi v9, v14
	v_bfe_u32 v14, v10, 16, 1
	v_add3_u32 v10, v10, v14, s27
	v_cmp_lt_f32_e32 vcc, 0, v11
	ds_write_b16_d16_hi v9, v10 offset:64
	s_lshl_b64 s[10:11], s[10:11], 11
	v_cndmask_b32_e32 v10, 0, v15, vcc
	v_mul_f32_e32 v11, v71, v10
	v_bfe_u32 v14, v11, 16, 1
	v_add3_u32 v14, v11, v14, s27
	v_or_b32_e32 v11, 0x480, v66
	v_rcp_f32_e32 v15, v12
	v_add_u32_e32 v11, v82, v11
	v_mul_f32_e32 v10, v55, v10
	ds_write_b16_d16_hi v11, v14
	v_bfe_u32 v14, v10, 16, 1
	v_add3_u32 v10, v10, v14, s27
	v_cmp_lt_f32_e32 vcc, 0, v12
	ds_write_b16_d16_hi v11, v10 offset:64
	v_and_b32_e32 v2, 56, v204
	v_cndmask_b32_e32 v10, 0, v15, vcc
	v_mul_f32_e32 v12, v72, v10
	v_bfe_u32 v14, v12, 16, 1
	v_rcp_f32_e32 v15, v13
	v_add3_u32 v14, v12, v14, s27
	v_or_b32_e32 v12, 0x500, v66
	v_add_u32_e32 v12, v82, v12
	v_mul_f32_e32 v10, v56, v10
	ds_write_b16_d16_hi v12, v14
	v_bfe_u32 v14, v10, 16, 1
	v_cmp_lt_f32_e32 vcc, 0, v13
	v_add3_u32 v10, v10, v14, s27
	ds_write_b16_d16_hi v12, v10 offset:64
	v_cndmask_b32_e32 v13, 0, v15, vcc
	v_mul_f32_e32 v10, v73, v13
	v_bfe_u32 v14, v10, 16, 1
	v_add3_u32 v50, v10, v14, s27
	ds_read_b128 v[14:17], v199 offset:192
	v_or_b32_e32 v10, 0x580, v66
	v_add_u32_e32 v10, v82, v10
	ds_write_b16_d16_hi v10, v50
	ds_read_b128 v[50:53], v199 offset:224
	s_waitcnt lgkmcnt(2)
	v_rcp_f32_e32 v55, v14
	v_mul_f32_e32 v13, v57, v13
	v_bfe_u32 v54, v13, 16, 1
	v_cmp_lt_f32_e32 vcc, 0, v14
	v_add3_u32 v13, v13, v54, s27
	ds_write_b16_d16_hi v10, v13 offset:64
	v_cndmask_b32_e32 v14, 0, v55, vcc
	v_mul_f32_e32 v13, v74, v14
	v_bfe_u32 v54, v13, 16, 1
	v_rcp_f32_e32 v55, v15
	v_add3_u32 v54, v13, v54, s27
	v_or_b32_e32 v13, 0x800, v66
	v_add_u32_e32 v13, v82, v13
	v_mul_f32_e32 v14, v58, v14
	ds_write_b16_d16_hi v13, v54
	v_bfe_u32 v54, v14, 16, 1
	v_cmp_lt_f32_e32 vcc, 0, v15
	v_add3_u32 v14, v14, v54, s27
	ds_write_b16_d16_hi v13, v14 offset:64
	v_cndmask_b32_e32 v15, 0, v55, vcc
	v_mul_f32_e32 v14, v75, v15
	v_bfe_u32 v54, v14, 16, 1
	v_rcp_f32_e32 v55, v16
	v_add3_u32 v54, v14, v54, s27
	v_or_b32_e32 v14, 0x880, v66
	v_add_u32_e32 v14, v82, v14
	v_mul_f32_e32 v15, v59, v15
	ds_write_b16_d16_hi v14, v54
	v_bfe_u32 v54, v15, 16, 1
	v_cmp_lt_f32_e32 vcc, 0, v16
	v_add3_u32 v15, v15, v54, s27
	ds_write_b16_d16_hi v14, v15 offset:64
	v_cndmask_b32_e32 v16, 0, v55, vcc
	v_mul_f32_e32 v15, v76, v16
	v_bfe_u32 v54, v15, 16, 1
	v_rcp_f32_e32 v55, v17
	v_add3_u32 v54, v15, v54, s27
	v_or_b32_e32 v15, 0x900, v66
	v_add_u32_e32 v15, v82, v15
	v_mul_f32_e32 v16, v60, v16
	ds_write_b16_d16_hi v15, v54
	v_bfe_u32 v54, v16, 16, 1
	v_cmp_lt_f32_e32 vcc, 0, v17
	v_add3_u32 v16, v16, v54, s27
	ds_write_b16_d16_hi v15, v16 offset:64
	v_cndmask_b32_e32 v17, 0, v55, vcc
	v_mul_f32_e32 v16, v77, v17
	v_bfe_u32 v54, v16, 16, 1
	s_waitcnt lgkmcnt(7)
	v_rcp_f32_e32 v55, v50
	v_add3_u32 v54, v16, v54, s27
	v_or_b32_e32 v16, 0x980, v66
	v_add_u32_e32 v16, v82, v16
	v_mul_f32_e32 v17, v61, v17
	ds_write_b16_d16_hi v16, v54
	v_bfe_u32 v54, v17, 16, 1
	v_cmp_lt_f32_e32 vcc, 0, v50
	v_add3_u32 v17, v17, v54, s27
	ds_write_b16_d16_hi v16, v17 offset:64
	v_cndmask_b32_e32 v50, 0, v55, vcc
	v_mul_f32_e32 v17, v78, v50
	v_bfe_u32 v54, v17, 16, 1
	v_rcp_f32_e32 v55, v51
	v_add3_u32 v54, v17, v54, s27
	v_or_b32_e32 v17, 0xc00, v66
	v_add_u32_e32 v17, v82, v17
	v_mul_f32_e32 v50, v62, v50
	ds_write_b16_d16_hi v17, v54
	v_bfe_u32 v54, v50, 16, 1
	v_cmp_lt_f32_e32 vcc, 0, v51
	v_add3_u32 v50, v50, v54, s27
	ds_write_b16_d16_hi v17, v50 offset:64
	v_cndmask_b32_e32 v51, 0, v55, vcc
	v_mul_f32_e32 v50, v79, v51
	v_bfe_u32 v54, v50, 16, 1
	v_rcp_f32_e32 v55, v52
	v_add3_u32 v54, v50, v54, s27
	v_or_b32_e32 v50, 0xc80, v66
	v_add_u32_e32 v50, v82, v50
	v_mul_f32_e32 v51, v63, v51
	ds_write_b16_d16_hi v50, v54
	v_bfe_u32 v54, v51, 16, 1
	v_cmp_lt_f32_e32 vcc, 0, v52
	v_add3_u32 v51, v51, v54, s27
	ds_write_b16_d16_hi v50, v51 offset:64
	v_cndmask_b32_e32 v52, 0, v55, vcc
	v_mul_f32_e32 v51, v80, v52
	v_bfe_u32 v54, v51, 16, 1
	v_rcp_f32_e32 v55, v53
	v_add3_u32 v54, v51, v54, s27
	v_or_b32_e32 v51, 0xd00, v66
	v_add_u32_e32 v51, v82, v51
	v_mul_f32_e32 v52, v64, v52
	ds_write_b16_d16_hi v51, v54
	v_bfe_u32 v54, v52, 16, 1
	v_cmp_lt_f32_e32 vcc, 0, v53
	v_add3_u32 v52, v52, v54, s27
	ds_write_b16_d16_hi v51, v52 offset:64
	v_cndmask_b32_e32 v53, 0, v55, vcc
	v_mul_f32_e32 v52, v81, v53
	v_bfe_u32 v54, v52, 16, 1
	v_add3_u32 v54, v52, v54, s27
	v_or_b32_e32 v52, 0xd80, v66
	v_add_u32_e32 v52, v82, v52
	v_mul_f32_e32 v53, v65, v53
	ds_write_b16_d16_hi v52, v54
	v_bfe_u32 v54, v53, 16, 1
	v_lshrrev_b32_e32 v4, 3, v205
	s_add_u32 s12, s10, s30
	v_lshlrev_b32_e32 v2, 1, v2
	v_add3_u32 v53, v53, v54, s27
	s_addc_u32 s6, s11, 0
	v_add_u32_e32 v83, s13, v2
	ds_write_b16_d16_hi v52, v53 offset:64
	v_lshlrev_b32_e32 v53, 7, v4
	s_waitcnt lgkmcnt(0)
	v_or_b32_e32 v68, s12, v4
	v_mov_b32_e32 v69, s6
	v_add_u32_e32 v55, v83, v53
	ds_read_b128 v[58:61], v55
	v_lshlrev_b64 v[56:57], 10, v[68:69]
	v_lshl_add_u64 v[56:57], s[4:5], 0, v[56:57]
	v_or_b32_e32 v53, 8, v4
	v_lshl_add_u64 v[56:57], v[56:57], 0, s[8:9]
	v_lshlrev_b32_e32 v54, 7, v53
	v_lshl_add_u64 v[66:67], v[56:57], 0, v[2:3]
	v_add_u32_e32 v57, v83, v54
	ds_read_b128 v[62:65], v57
	v_or_b32_e32 v68, s12, v53
	s_waitcnt lgkmcnt(1)
	global_store_dwordx4 v[66:67], v[58:61], off nt
	v_or_b32_e32 v56, 16, v4
	v_lshlrev_b32_e32 v54, 7, v56
	v_lshlrev_b64 v[58:59], 10, v[68:69]
	v_lshl_add_u64 v[58:59], s[4:5], 0, v[58:59]
	v_lshl_add_u64 v[58:59], v[58:59], 0, s[8:9]
	v_lshl_add_u64 v[58:59], v[58:59], 0, v[2:3]
	s_waitcnt lgkmcnt(0)
	global_store_dwordx4 v[58:59], v[62:65], off nt
	v_add_u32_e32 v58, v83, v54
	v_or_b32_e32 v68, s12, v56
	ds_read_b128 v[60:63], v58
	v_lshlrev_b64 v[64:65], 10, v[68:69]
	v_or_b32_e32 v54, 24, v4
	v_lshl_add_u64 v[64:65], s[4:5], 0, v[64:65]
	v_lshlrev_b32_e32 v59, 7, v54
	v_lshl_add_u64 v[64:65], v[64:65], 0, s[8:9]
	v_add_u32_e32 v59, v83, v59
	v_lshl_add_u64 v[70:71], v[64:65], 0, v[2:3]
	ds_read_b128 v[64:67], v59
	v_or_b32_e32 v68, s12, v54
	s_waitcnt lgkmcnt(1)
	global_store_dwordx4 v[70:71], v[60:63], off nt
	s_nop 1
	v_lshlrev_b64 v[60:61], 10, v[68:69]
	v_lshl_add_u64 v[60:61], s[4:5], 0, v[60:61]
	v_lshl_add_u64 v[60:61], v[60:61], 0, s[8:9]
	v_lshl_add_u64 v[60:61], v[60:61], 0, v[2:3]
	s_waitcnt lgkmcnt(0)
	global_store_dwordx4 v[60:61], v[64:67], off nt
	s_waitcnt lgkmcnt(0)
	v_mov_b32_e32 v60, v201
	s_nop 1
	v_permlane32_swap_b32_e32 v201, v60
	s_and_saveexec_b64 s[10:11], s[2:3]
	s_cbranch_execz .LBB0_513
	v_add_f32_e32 v60, v201, v60
	ds_write_b32 v200, v60 offset:128
	s_branch .LBB0_513

.LBB0_556:
	s_or_b64 exec, exec, s[10:11]
	v_cvt_pk_bf16_f32 v182, v10, v11
	v_cvt_pk_bf16_f32 v183, v8, v9
	v_cvt_pk_bf16_f32 v184, v6, v7
	v_cvt_pk_bf16_f32 v185, v4, v5
	ds_read_b64_tr_b16 v[4:5], v179 offset:16384
	ds_read_b64_tr_b16 v[6:7], v179 offset:16896
	v_cvt_pk_bf16_f32 v186, v2, v3
	s_waitcnt lgkmcnt(0)
	v_mfma_f32_32x32x16_bf16 v[2:17], v[182:185], v[4:7], 0
	ds_read_b64_tr_b16 v[190:191], v179 offset:17408
	ds_read_b64_tr_b16 v[192:193], v179 offset:17920
	v_cvt_pk_bf16_f32 v187, v24, v25
	v_cvt_pk_bf16_f32 v188, v26, v27
	v_cvt_pk_bf16_f32 v189, v32, v33
	v_cvt_pk_bf16_f32 v92, v92, v93
	v_cvt_pk_bf16_f32 v93, v94, v95
	v_cvt_pk_bf16_f32 v94, v96, v97
	s_waitcnt lgkmcnt(0)
	v_mfma_f32_32x32x16_bf16 v[2:17], v[186:189], v[190:193], v[2:17]
	v_cvt_pk_bf16_f32 v95, v28, v29
	ds_read_b64_tr_b16 v[24:25], v179 offset:18432
	ds_read_b64_tr_b16 v[26:27], v179 offset:18944
	v_cvt_pk_bf16_f32 v190, v30, v31
	ds_read_b64_tr_b16 v[28:29], v179 offset:19456
	ds_read_b64_tr_b16 v[30:31], v179 offset:19968
	v_cvt_pk_bf16_f32 v191, v18, v19
	v_cvt_pk_bf16_f32 v192, v20, v21
	v_cvt_pk_bf16_f32 v193, v22, v23
	s_waitcnt lgkmcnt(2)
	v_mfma_f32_32x32x16_bf16 v[2:17], v[92:95], v[24:27], v[2:17]
	ds_read_b64_tr_b16 v[18:19], v179 offset:20480
	ds_read_b64_tr_b16 v[20:21], v179 offset:20992
	ds_read_b64_tr_b16 v[194:195], v179 offset:21504
	ds_read_b64_tr_b16 v[196:197], v179 offset:22016
	v_cvt_pk_bf16_f32 v56, v56, v57
	v_cvt_pk_bf16_f32 v57, v40, v41
	v_cvt_pk_bf16_f32 v40, v50, v51
	v_cvt_pk_bf16_f32 v41, v52, v53
	s_lshl_b32 s10, s39, 12
	s_add_i32 s10, s10, 0
	s_waitcnt lgkmcnt(4)
	v_mfma_f32_32x32x16_bf16 v[2:17], v[190:193], v[28:31], v[2:17]
	s_waitcnt lgkmcnt(2)
	v_mfma_f32_32x32x16_bf16 v[18:33], v[182:185], v[18:21], 0
	s_waitcnt lgkmcnt(0)
	v_mfma_f32_32x32x16_bf16 v[18:33], v[186:189], v[194:197], v[18:33]
	ds_read_b64_tr_b16 v[182:183], v179 offset:22528
	ds_read_b64_tr_b16 v[184:185], v179 offset:23040
	ds_read_b64_tr_b16 v[186:187], v179 offset:23552
	ds_read_b64_tr_b16 v[188:189], v179 offset:24064
	s_waitcnt lgkmcnt(2)
	v_mfma_f32_32x32x16_bf16 v[18:33], v[92:95], v[182:185], v[18:33]
	v_cvt_pk_bf16_f32 v92, v64, v65
	v_cvt_pk_bf16_f32 v93, v62, v63
	v_cvt_pk_bf16_f32 v94, v60, v61
	v_cvt_pk_bf16_f32 v95, v58, v59
	ds_read_b64_tr_b16 v[58:59], v179 offset:24576
	ds_read_b64_tr_b16 v[60:61], v179 offset:25088
	ds_read_b64_tr_b16 v[62:63], v179 offset:25600
	ds_read_b64_tr_b16 v[64:65], v179 offset:26112
	s_waitcnt lgkmcnt(2)
	v_mfma_f32_32x32x16_bf16 v[2:17], v[92:95], v[58:61], v[2:17]
	v_cvt_pk_bf16_f32 v58, v42, v43
	v_cvt_pk_bf16_f32 v59, v48, v49
	v_cvt_pk_bf16_f32 v42, v54, v55
	v_cvt_pk_bf16_f32 v43, v44, v45
	ds_read_b64_tr_b16 v[48:49], v179 offset:26624
	ds_read_b64_tr_b16 v[50:51], v179 offset:27136
	v_cvt_pk_bf16_f32 v44, v46, v47
	ds_read_b64_tr_b16 v[52:53], v179 offset:27648
	ds_read_b64_tr_b16 v[54:55], v179 offset:28160
	s_waitcnt lgkmcnt(4)
	v_mfma_f32_32x32x16_bf16 v[2:17], v[56:59], v[62:65], v[2:17]
	v_cvt_pk_bf16_f32 v45, v34, v35
	v_cvt_pk_bf16_f32 v46, v36, v37
	v_cvt_pk_bf16_f32 v47, v38, v39
	v_mfma_f32_32x32x16_bf16 v[18:33], v[190:193], v[186:189], v[18:33]
	s_waitcnt lgkmcnt(2)
	v_mfma_f32_32x32x16_bf16 v[2:17], v[40:43], v[48:51], v[2:17]
	ds_read_b64_tr_b16 v[34:35], v179 offset:28672
	ds_read_b64_tr_b16 v[36:37], v179 offset:29184
	ds_read_b64_tr_b16 v[48:49], v179 offset:29696
	ds_read_b64_tr_b16 v[50:51], v179 offset:30208
	s_waitcnt lgkmcnt(2)
	v_mfma_f32_32x32x16_bf16 v[18:33], v[92:95], v[34:37], v[18:33]
	s_waitcnt lgkmcnt(0)
	v_mfma_f32_32x32x16_bf16 v[18:33], v[56:59], v[48:51], v[18:33]
	ds_read_b64_tr_b16 v[34:35], v179 offset:30720
	ds_read_b64_tr_b16 v[36:37], v179 offset:31232
	ds_read_b64_tr_b16 v[48:49], v179 offset:31744
	ds_read_b64_tr_b16 v[50:51], v179 offset:32256
	s_waitcnt lgkmcnt(2)
	v_mfma_f32_32x32x16_bf16 v[18:33], v[40:43], v[34:37], v[18:33]
	v_lshlrev_b32_e32 v34, 1, v1
	v_add3_u32 v34, s10, v159, v34
	v_mfma_f32_32x32x16_bf16 v[2:17], v[44:47], v[52:55], v[2:17]
	s_waitcnt lgkmcnt(0)
	v_mfma_f32_32x32x16_bf16 v[18:33], v[44:47], v[48:51], v[18:33]
	s_nop 9
	v_bfe_u32 v35, v2, 16, 1
	v_add3_u32 v2, v2, v35, s28
	ds_write_b16_d16_hi v34, v2 offset:35328
	v_bfe_u32 v2, v18, 16, 1
	v_add3_u32 v2, v18, v2, s28
	ds_write_b16_d16_hi v34, v2 offset:35392
	v_bfe_u32 v2, v3, 16, 1
	v_add3_u32 v2, v3, v2, s28
	ds_write_b16_d16_hi v34, v2 offset:35456
	v_bfe_u32 v2, v19, 16, 1
	v_add3_u32 v2, v19, v2, s28
	ds_write_b16_d16_hi v34, v2 offset:35520
	v_bfe_u32 v2, v4, 16, 1
	v_add3_u32 v2, v4, v2, s28
	ds_write_b16_d16_hi v34, v2 offset:35584
	v_bfe_u32 v2, v20, 16, 1
	v_add3_u32 v2, v20, v2, s28
	ds_write_b16_d16_hi v34, v2 offset:35648
	v_bfe_u32 v2, v5, 16, 1
	v_add3_u32 v2, v5, v2, s28
	ds_write_b16_d16_hi v34, v2 offset:35712
	v_bfe_u32 v2, v21, 16, 1
	v_add3_u32 v2, v21, v2, s28
	ds_write_b16_d16_hi v34, v2 offset:35776
	v_bfe_u32 v2, v6, 16, 1
	v_add3_u32 v2, v6, v2, s28
	ds_write_b16_d16_hi v34, v2 offset:36352
	v_bfe_u32 v2, v22, 16, 1
	v_add3_u32 v2, v22, v2, s28
	ds_write_b16_d16_hi v34, v2 offset:36416
	v_bfe_u32 v2, v7, 16, 1
	v_add3_u32 v2, v7, v2, s28
	ds_write_b16_d16_hi v34, v2 offset:36480
	v_bfe_u32 v2, v23, 16, 1
	v_add3_u32 v2, v23, v2, s28
	ds_write_b16_d16_hi v34, v2 offset:36544
	v_bfe_u32 v2, v8, 16, 1
	v_add3_u32 v2, v8, v2, s28
	ds_write_b16_d16_hi v34, v2 offset:36608
	v_bfe_u32 v2, v24, 16, 1
	v_add3_u32 v2, v24, v2, s28
	ds_write_b16_d16_hi v34, v2 offset:36672
	v_bfe_u32 v2, v9, 16, 1
	v_add3_u32 v2, v9, v2, s28
	ds_write_b16_d16_hi v34, v2 offset:36736
	v_bfe_u32 v2, v25, 16, 1
	v_add3_u32 v2, v25, v2, s28
	ds_write_b16_d16_hi v34, v2 offset:36800
	v_bfe_u32 v2, v10, 16, 1
	v_add3_u32 v2, v10, v2, s28
	ds_write_b16_d16_hi v34, v2 offset:37376
	v_bfe_u32 v2, v26, 16, 1
	v_add3_u32 v2, v26, v2, s28
	ds_write_b16_d16_hi v34, v2 offset:37440
	v_bfe_u32 v2, v11, 16, 1
	v_add3_u32 v2, v11, v2, s28
	ds_write_b16_d16_hi v34, v2 offset:37504
	v_bfe_u32 v2, v27, 16, 1
	v_add3_u32 v2, v27, v2, s28
	ds_write_b16_d16_hi v34, v2 offset:37568
	v_bfe_u32 v2, v12, 16, 1
	v_add3_u32 v2, v12, v2, s28
	ds_write_b16_d16_hi v34, v2 offset:37632
	v_bfe_u32 v2, v28, 16, 1
	v_add3_u32 v2, v28, v2, s28
	ds_write_b16_d16_hi v34, v2 offset:37696
	v_bfe_u32 v2, v13, 16, 1
	v_add3_u32 v2, v13, v2, s28
	ds_write_b16_d16_hi v34, v2 offset:37760
	v_bfe_u32 v2, v29, 16, 1
	v_add3_u32 v2, v29, v2, s28
	ds_write_b16_d16_hi v34, v2 offset:37824
	v_bfe_u32 v2, v14, 16, 1
	v_add3_u32 v2, v14, v2, s28
	ds_write_b16_d16_hi v34, v2 offset:38400
	v_bfe_u32 v2, v30, 16, 1
	v_add3_u32 v2, v30, v2, s28
	ds_write_b16_d16_hi v34, v2 offset:38464
	v_bfe_u32 v2, v15, 16, 1
	v_add3_u32 v2, v15, v2, s28
	ds_write_b16_d16_hi v34, v2 offset:38528
	v_bfe_u32 v2, v31, 16, 1
	v_add3_u32 v2, v31, v2, s28
	ds_write_b16_d16_hi v34, v2 offset:38592
	v_bfe_u32 v2, v16, 16, 1
	v_add3_u32 v2, v16, v2, s28
	ds_write_b16_d16_hi v34, v2 offset:38656
	v_bfe_u32 v2, v32, 16, 1
	v_add3_u32 v2, v32, v2, s28
	ds_write_b16_d16_hi v34, v2 offset:38720
	v_bfe_u32 v2, v17, 16, 1
	v_add3_u32 v2, v17, v2, s28
	ds_write_b16_d16_hi v34, v2 offset:38784
	v_bfe_u32 v2, v33, 16, 1
	v_add3_u32 v2, v33, v2, s28
	v_lshl_add_u32 v14, v161, 1, s10
	s_or_b32 s10, s16, s34
	ds_write_b16_d16_hi v34, v2 offset:38848
	s_add_u32 s10, s10, s35
	v_or_b32_e32 v2, s38, v162
	s_waitcnt lgkmcnt(0)
	s_addc_u32 s11, s17, 0
	v_lshlrev_b32_e32 v76, 7, v2
	v_add_u32_e32 v2, v14, v163
	ds_read_b128 v[2:5], v2 offset:35328
	v_mov_b32_e32 v7, s11
	v_or_b32_e32 v6, s10, v74
	v_lshl_add_u64 v[10:11], v[78:79], 0, v[76:77]
	v_lshlrev_b64 v[6:7], 10, v[6:7]
	v_lshl_add_u64 v[12:13], v[10:11], 0, v[6:7]
	v_add_u32_e32 v6, v14, v164
	ds_read_b128 v[6:9], v6 offset:35328
	s_waitcnt lgkmcnt(1)
	global_store_dwordx4 v[12:13], v[2:5], off nt
	s_cmp_lt_u32 s30, 3
	s_nop 0
	v_mov_b32_e32 v3, s11
	v_or_b32_e32 v2, s10, v80
	v_lshlrev_b64 v[2:3], 10, v[2:3]
	v_lshl_add_u64 v[2:3], v[10:11], 0, v[2:3]
	s_waitcnt lgkmcnt(0)
	global_store_dwordx4 v[2:3], v[6:9], off nt
	v_add_u32_e32 v2, v14, v165
	ds_read_b128 v[2:5], v2 offset:35328
	v_mov_b32_e32 v7, s11
	v_or_b32_e32 v6, s10, v82
	v_lshlrev_b64 v[6:7], 10, v[6:7]
	v_lshl_add_u64 v[12:13], v[10:11], 0, v[6:7]
	v_add_u32_e32 v6, v14, v166
	ds_read_b128 v[6:9], v6 offset:35328
	s_waitcnt lgkmcnt(1)
	global_store_dwordx4 v[12:13], v[2:5], off nt
	v_mov_b32_e32 v12, 0
	v_mov_b32_e32 v13, 0
	v_mov_b32_e32 v3, s11
	v_or_b32_e32 v2, s10, v84
	v_lshlrev_b64 v[2:3], 10, v[2:3]
	v_lshl_add_u64 v[2:3], v[10:11], 0, v[2:3]
	s_waitcnt lgkmcnt(0)
	global_store_dwordx4 v[2:3], v[6:9], off nt
	s_waitcnt lgkmcnt(0)
	v_mov_b32_e32 v10, 0
	v_mov_b32_e32 v11, 0
	s_cbranch_scc1 .LBB0_564
	v_lshlrev_b32_e32 v2, 2, v167
	v_add3_u32 v2, s40, v163, v2
	ds_read_b128 v[4:7], v2
	s_add_i32 s16, s30, -2
	s_cmp_lt_u32 s16, 2
	s_waitcnt lgkmcnt(0)
	v_mov_b32_e32 v76, v5
	v_mov_b32_e32 v5, v77
	v_lshlrev_b64 v[2:3], 5, v[4:5]
	v_lshlrev_b64 v[4:5], 5, v[76:77]
	v_mov_b32_e32 v76, v7
	v_mov_b32_e32 v7, v77
	v_lshlrev_b64 v[6:7], 5, v[6:7]
	v_lshlrev_b64 v[8:9], 5, v[76:77]
	v_or_b32_e32 v4, v4, v66
	v_or_b32_e32 v2, v2, v68
	v_or_b32_e32 v8, v8, v70
	v_or_b32_e32 v6, v6, v72
	s_cbranch_scc1 .LBB0_561
	s_and_b32 s10, s33, 1
	s_sub_i32 s16, s16, s10
	s_mov_b32 s11, 1
	v_mov_b32_e32 v10, v2
	v_mov_b32_e32 v11, v3
	v_mov_b32_e32 v12, v4
	v_mov_b32_e32 v13, v5
	v_mov_b32_e32 v14, v6
	v_mov_b32_e32 v15, v7
	v_mov_b32_e32 v16, v8
	v_mov_b32_e32 v17, v9
	v_add_u32_e32 v19, s31, v175
	s_mov_b32 s17, 2
	v_mov_b32_e32 v18, 0
	s_mov_b32 s33, s16
	v_mov_b32_e32 v20, 0
	v_mov_b32_e32 v21, 0
	v_mov_b32_e32 v22, 0
	v_mov_b32_e32 v23, 0
	v_mov_b32_e32 v24, 0
	v_mov_b32_e32 v25, 0
	v_mov_b32_e32 v26, 0

.LBB0_635:
	s_or_b64 exec, exec, s[6:7]
	s_waitcnt lgkmcnt(0)
	ds_read_b128 v[34:37], v165 offset:128
	ds_read_b128 v[38:41], v165 offset:160
	s_or_b32 s2, s11, 32
	s_waitcnt lgkmcnt(1)
	v_rcp_f32_e32 v42, v34
	v_cmp_lt_f32_e32 vcc, 0, v34
	v_rcp_f32_e32 v43, v35
	s_nop 0
	v_cndmask_b32_e32 v34, 0, v42, vcc
	v_mul_f32_e32 v18, v18, v34
	v_mul_f32_e32 v2, v2, v34
	v_bfe_u32 v34, v18, 16, 1
	v_bfe_u32 v42, v2, 16, 1
	v_add3_u32 v18, v18, v34, s40
	v_add3_u32 v2, v2, v42, s40
	v_cmp_lt_f32_e32 vcc, 0, v35
	ds_write_b16_d16_hi v71, v18
	ds_write_b16_d16_hi v71, v2 offset:64
	v_cndmask_b32_e32 v2, 0, v43, vcc
	v_mul_f32_e32 v18, v19, v2
	v_bfe_u32 v19, v18, 16, 1
	v_add3_u32 v18, v18, v19, s40
	ds_write_b16_d16_hi v72, v18
	v_rcp_f32_e32 v18, v36
	v_mul_f32_e32 v2, v3, v2
	v_bfe_u32 v3, v2, 16, 1
	v_add3_u32 v2, v2, v3, s40
	v_cmp_lt_f32_e32 vcc, 0, v36
	ds_write_b16_d16_hi v72, v2 offset:64
	v_mov_b32_e32 v71, s10
	v_cndmask_b32_e32 v2, 0, v18, vcc
	v_mul_f32_e32 v3, v20, v2
	v_bfe_u32 v18, v3, 16, 1
	v_mul_f32_e32 v2, v4, v2
	v_rcp_f32_e32 v4, v37
	v_add3_u32 v3, v3, v18, s40
	ds_write_b16_d16_hi v73, v3
	v_bfe_u32 v3, v2, 16, 1
	v_add3_u32 v2, v2, v3, s40
	v_cmp_lt_f32_e32 vcc, 0, v37
	ds_write_b16_d16_hi v73, v2 offset:64
	s_nop 0
	v_cndmask_b32_e32 v2, 0, v4, vcc
	v_mul_f32_e32 v3, v21, v2
	v_bfe_u32 v4, v3, 16, 1
	v_add3_u32 v3, v3, v4, s40
	s_waitcnt lgkmcnt(6)
	v_rcp_f32_e32 v4, v38
	v_mul_f32_e32 v2, v5, v2
	ds_write_b16_d16_hi v53, v3
	v_bfe_u32 v3, v2, 16, 1
	v_add3_u32 v2, v2, v3, s40
	v_cmp_lt_f32_e32 vcc, 0, v38
	ds_write_b16_d16_hi v53, v2 offset:64
	s_nop 0
	v_cndmask_b32_e32 v2, 0, v4, vcc
	v_mul_f32_e32 v3, v22, v2
	v_bfe_u32 v4, v3, 16, 1
	v_add3_u32 v3, v3, v4, s40
	v_rcp_f32_e32 v4, v39
	v_mul_f32_e32 v2, v6, v2
	ds_write_b16_d16_hi v74, v3
	v_bfe_u32 v3, v2, 16, 1
	v_add3_u32 v2, v2, v3, s40
	v_cmp_lt_f32_e32 vcc, 0, v39
	ds_write_b16_d16_hi v74, v2 offset:64
	s_nop 0
	v_cndmask_b32_e32 v2, 0, v4, vcc
	v_mul_f32_e32 v3, v23, v2
	v_bfe_u32 v4, v3, 16, 1
	v_add3_u32 v3, v3, v4, s40
	v_rcp_f32_e32 v4, v40
	v_mul_f32_e32 v2, v7, v2
	ds_write_b16_d16_hi v75, v3
	v_bfe_u32 v3, v2, 16, 1
	v_add3_u32 v2, v2, v3, s40
	v_cmp_lt_f32_e32 vcc, 0, v40
	ds_write_b16_d16_hi v75, v2 offset:64
	s_nop 0
	v_cndmask_b32_e32 v2, 0, v4, vcc
	v_mul_f32_e32 v3, v24, v2
	v_bfe_u32 v4, v3, 16, 1
	v_add3_u32 v3, v3, v4, s40
	v_rcp_f32_e32 v4, v41
	v_mul_f32_e32 v2, v8, v2
	ds_write_b16_d16_hi v76, v3
	v_bfe_u32 v3, v2, 16, 1
	v_cmp_lt_f32_e32 vcc, 0, v41
	v_add3_u32 v2, v2, v3, s40
	ds_write_b16_d16_hi v76, v2 offset:64
	v_cndmask_b32_e32 v6, 0, v4, vcc
	v_mul_f32_e32 v2, v25, v6
	v_bfe_u32 v3, v2, 16, 1
	v_add3_u32 v7, v2, v3, s40
	ds_read_b128 v[2:5], v165 offset:192
	ds_write_b16_d16_hi v57, v7
	v_mul_f32_e32 v18, v9, v6
	ds_read_b128 v[6:9], v165 offset:224
	v_bfe_u32 v19, v18, 16, 1
	s_waitcnt lgkmcnt(2)
	v_rcp_f32_e32 v20, v2
	v_cmp_lt_f32_e32 vcc, 0, v2
	v_add3_u32 v18, v18, v19, s40
	ds_write_b16_d16_hi v57, v18 offset:64
	v_cndmask_b32_e32 v2, 0, v20, vcc
	v_mul_f32_e32 v18, v26, v2
	v_bfe_u32 v19, v18, 16, 1
	v_add3_u32 v18, v18, v19, s40
	ds_write_b16_d16_hi v77, v18
	v_rcp_f32_e32 v18, v3
	v_mul_f32_e32 v2, v10, v2
	v_bfe_u32 v10, v2, 16, 1
	v_add3_u32 v2, v2, v10, s40
	v_cmp_lt_f32_e32 vcc, 0, v3
	ds_write_b16_d16_hi v77, v2 offset:64
	v_or_b32_e32 v26, s2, v85
	v_cndmask_b32_e32 v2, 0, v18, vcc
	v_mul_f32_e32 v3, v27, v2
	v_bfe_u32 v10, v3, 16, 1
	v_add3_u32 v3, v3, v10, s40
	v_rcp_f32_e32 v10, v4
	v_mul_f32_e32 v2, v11, v2
	ds_write_b16_d16_hi v78, v3
	v_bfe_u32 v3, v2, 16, 1
	v_add3_u32 v2, v2, v3, s40
	v_cmp_lt_f32_e32 vcc, 0, v4
	ds_write_b16_d16_hi v78, v2 offset:64
	v_mov_b32_e32 v27, s10
	v_cndmask_b32_e32 v2, 0, v10, vcc
	v_mul_f32_e32 v3, v28, v2
	v_bfe_u32 v4, v3, 16, 1
	v_add3_u32 v3, v3, v4, s40
	v_rcp_f32_e32 v4, v5
	v_mul_f32_e32 v2, v12, v2
	ds_write_b16_d16_hi v79, v3
	v_bfe_u32 v3, v2, 16, 1
	v_add3_u32 v2, v2, v3, s40
	v_cmp_lt_f32_e32 vcc, 0, v5
	ds_write_b16_d16_hi v79, v2 offset:64
	v_or_b32_e32 v28, s2, v84
	v_cndmask_b32_e32 v2, 0, v4, vcc
	v_mul_f32_e32 v3, v29, v2
	v_bfe_u32 v4, v3, 16, 1
	v_add3_u32 v3, v3, v4, s40
	s_waitcnt lgkmcnt(7)
	v_rcp_f32_e32 v4, v6
	v_mul_f32_e32 v2, v13, v2
	ds_write_b16_d16_hi v80, v3
	v_bfe_u32 v3, v2, 16, 1
	v_add3_u32 v2, v2, v3, s40
	v_cmp_lt_f32_e32 vcc, 0, v6
	ds_write_b16_d16_hi v80, v2 offset:64
	v_mov_b32_e32 v29, s10
	v_cndmask_b32_e32 v2, 0, v4, vcc
	v_mul_f32_e32 v3, v30, v2
	v_bfe_u32 v4, v3, 16, 1
	v_add3_u32 v3, v3, v4, s40
	v_rcp_f32_e32 v4, v7
	v_mul_f32_e32 v2, v14, v2
	ds_write_b16_d16_hi v81, v3
	v_bfe_u32 v3, v2, 16, 1
	v_add3_u32 v2, v2, v3, s40
	v_cmp_lt_f32_e32 vcc, 0, v7
	ds_write_b16_d16_hi v81, v2 offset:64
	s_nop 0
	v_cndmask_b32_e32 v2, 0, v4, vcc
	v_mul_f32_e32 v3, v31, v2
	v_bfe_u32 v4, v3, 16, 1
	v_add3_u32 v3, v3, v4, s40
	v_rcp_f32_e32 v4, v8
	v_mul_f32_e32 v2, v15, v2
	ds_write_b16_d16_hi v82, v3
	v_bfe_u32 v3, v2, 16, 1
	v_add3_u32 v2, v2, v3, s40
	v_cmp_lt_f32_e32 vcc, 0, v8
	ds_write_b16_d16_hi v82, v2 offset:64
	s_nop 0
	v_cndmask_b32_e32 v2, 0, v4, vcc
	v_mul_f32_e32 v3, v32, v2
	v_bfe_u32 v4, v3, 16, 1
	v_add3_u32 v3, v3, v4, s40
	v_rcp_f32_e32 v4, v9
	v_mul_f32_e32 v2, v16, v2
	ds_write_b16_d16_hi v64, v3
	v_bfe_u32 v3, v2, 16, 1
	v_add3_u32 v2, v2, v3, s40
	v_cmp_lt_f32_e32 vcc, 0, v9
	ds_write_b16_d16_hi v64, v2 offset:64
	v_or_b32_e32 v64, s2, v70
	v_cndmask_b32_e32 v2, 0, v4, vcc
	v_mul_f32_e32 v3, v33, v2
	v_bfe_u32 v4, v3, 16, 1
	v_add3_u32 v3, v3, v4, s40
	v_mul_f32_e32 v2, v17, v2
	ds_write_b16_d16_hi v65, v3
	v_bfe_u32 v3, v2, 16, 1
	v_add3_u32 v2, v2, v3, s40
	ds_write_b16_d16_hi v65, v2 offset:64
	v_mov_b32_e32 v65, s10
	v_lshlrev_b64 v[2:3], 10, v[64:65]
	s_waitcnt lgkmcnt(0)
	v_lshl_add_u64 v[4:5], v[66:67], 0, v[2:3]
	v_lshl_add_u64 v[2:3], v[68:69], 0, v[2:3]
	global_load_dwordx4 v[30:33], v[4:5], off
	global_load_dwordx4 v[34:37], v[2:3], off
	v_lshlrev_b64 v[4:5], 7, v[64:65]
	v_lshl_add_u64 v[2:3], s[8:9], 0, v[4:5]
	global_load_dwordx3 v[54:56], v[2:3], off
	v_or_b32_e32 v70, s2, v83
	v_lshlrev_b64 v[2:3], 10, v[70:71]
	v_lshl_add_u64 v[4:5], v[66:67], 0, v[2:3]
	v_lshl_add_u64 v[2:3], v[68:69], 0, v[2:3]
	global_load_dwordx4 v[38:41], v[4:5], off
	global_load_dwordx4 v[42:45], v[2:3], off
	v_lshlrev_b64 v[4:5], 7, v[70:71]
	v_lshl_add_u64 v[2:3], s[8:9], 0, v[4:5]
	global_load_dwordx3 v[60:62], v[2:3], off
	v_lshlrev_b64 v[2:3], 7, v[28:29]
	v_lshl_add_u64 v[2:3], s[8:9], 0, v[2:3]
	v_lshlrev_b64 v[4:5], 10, v[28:29]
	v_lshl_add_u64 v[6:7], v[66:67], 0, v[4:5]
	global_load_dwordx3 v[22:24], v[2:3], off
	global_load_dwordx4 v[10:13], v[6:7], off
	v_lshl_add_u64 v[2:3], v[68:69], 0, v[4:5]
	v_lshlrev_b64 v[4:5], 7, v[26:27]
	v_lshl_add_u64 v[4:5], s[8:9], 0, v[4:5]
	global_load_dwordx4 v[14:17], v[2:3], off
	global_load_dwordx3 v[18:20], v[4:5], off
	v_lshlrev_b64 v[2:3], 10, v[26:27]
	v_lshl_add_u64 v[4:5], v[66:67], 0, v[2:3]
	v_lshl_add_u64 v[2:3], v[68:69], 0, v[2:3]
	ds_read_b128 v[46:49], v86
	global_load_dwordx4 v[6:9], v[4:5], off
	s_nop 0
	global_load_dwordx4 v[2:5], v[2:3], off
	ds_read_b128 v[50:53], v87
	s_mov_b64 s[2:3], 0
	s_waitcnt lgkmcnt(1)
	v_and_b32_e32 v69, 0xffff0000, v46
	v_lshlrev_b32_e32 v66, 16, v46
	s_waitcnt vmcnt(11)
	v_lshlrev_b32_e32 v68, 16, v30
	v_and_b32_e32 v67, 0xffff0000, v30
	s_waitcnt vmcnt(10)
	v_lshlrev_b32_e32 v72, 16, v34
	v_and_b32_e32 v73, 0xffff0000, v34
	s_waitcnt vmcnt(9)
	v_mov_b32_e32 v34, v56
	v_pk_mul_f32 v[56:57], v[54:55], v[68:69]
	v_lshlrev_b32_e32 v46, 16, v31
	v_pk_fma_f32 v[56:57], v[54:55], v[66:67], v[56:57] op_sel:[1,0,0] op_sel_hi:[0,1,1]
	v_pk_fma_f32 v[56:57], v[34:35], v[72:73], v[56:57] op_sel_hi:[0,1,1]
	v_cvt_pk_bf16_f32 v30, v56, v57
	v_lshlrev_b32_e32 v56, 16, v47
	v_and_b32_e32 v47, 0xffff0000, v47
	v_and_b32_e32 v57, 0xffff0000, v31
	v_pk_mul_f32 v[46:47], v[54:55], v[46:47]
	v_lshlrev_b32_e32 v66, 16, v35
	v_and_b32_e32 v67, 0xffff0000, v35
	v_pk_fma_f32 v[46:47], v[54:55], v[56:57], v[46:47] op_sel:[1,0,0] op_sel_hi:[0,1,1]
	v_pk_fma_f32 v[46:47], v[34:35], v[66:67], v[46:47] op_sel_hi:[0,1,1]
	v_lshlrev_b32_e32 v56, 16, v32
	v_and_b32_e32 v57, 0xffff0000, v48
	v_cvt_pk_bf16_f32 v31, v46, v47
	v_lshlrev_b32_e32 v46, 16, v48
	v_and_b32_e32 v47, 0xffff0000, v32
	v_pk_mul_f32 v[56:57], v[54:55], v[56:57]
	v_lshlrev_b32_e32 v66, 16, v36
	v_and_b32_e32 v67, 0xffff0000, v36
	v_pk_fma_f32 v[46:47], v[54:55], v[46:47], v[56:57] op_sel:[1,0,0] op_sel_hi:[0,1,1]
	v_pk_fma_f32 v[46:47], v[34:35], v[66:67], v[46:47] op_sel_hi:[0,1,1]
	v_cvt_pk_bf16_f32 v32, v46, v47
	v_lshlrev_b32_e32 v46, 16, v49
	v_lshlrev_b32_e32 v48, 16, v33
	v_and_b32_e32 v49, 0xffff0000, v49
	v_and_b32_e32 v47, 0xffff0000, v33
	v_pk_mul_f32 v[48:49], v[54:55], v[48:49]
	v_lshlrev_b32_e32 v36, 16, v37
	v_pk_fma_f32 v[46:47], v[54:55], v[46:47], v[48:49] op_sel:[1,0,0] op_sel_hi:[0,1,1]
	v_and_b32_e32 v37, 0xffff0000, v37
	v_pk_fma_f32 v[34:35], v[34:35], v[36:37], v[46:47] op_sel_hi:[0,1,1]
	v_cvt_pk_bf16_f32 v33, v34, v35
	v_lshlrev_b64 v[34:35], 11, v[64:65]
	s_waitcnt vmcnt(8)
	v_lshlrev_b32_e32 v36, 16, v38
	s_waitcnt lgkmcnt(0)
	v_and_b32_e32 v37, 0xffff0000, v50
	v_lshl_add_u64 v[46:47], v[58:59], 0, v[34:35]
	v_lshlrev_b32_e32 v34, 16, v50
	v_and_b32_e32 v35, 0xffff0000, v38
	s_waitcnt vmcnt(6)
	v_pk_mul_f32 v[36:37], v[60:61], v[36:37]
	v_lshlrev_b32_e32 v48, 16, v42
	v_and_b32_e32 v49, 0xffff0000, v42
	v_mov_b32_e32 v38, v62
	v_pk_fma_f32 v[34:35], v[60:61], v[34:35], v[36:37] op_sel:[1,0,0] op_sel_hi:[0,1,1]
	v_pk_fma_f32 v[34:35], v[38:39], v[48:49], v[34:35] op_sel_hi:[0,1,1]
	v_lshlrev_b32_e32 v48, 16, v39
	v_and_b32_e32 v49, 0xffff0000, v51
	v_lshlrev_b32_e32 v36, 16, v51
	v_and_b32_e32 v37, 0xffff0000, v39
	v_pk_mul_f32 v[48:49], v[60:61], v[48:49]
	v_lshlrev_b32_e32 v42, 16, v43
	v_and_b32_e32 v43, 0xffff0000, v43
	v_pk_fma_f32 v[36:37], v[60:61], v[36:37], v[48:49] op_sel:[1,0,0] op_sel_hi:[0,1,1]
	v_pk_fma_f32 v[36:37], v[38:39], v[42:43], v[36:37] op_sel_hi:[0,1,1]
	v_lshlrev_b32_e32 v42, 16, v40
	v_and_b32_e32 v43, 0xffff0000, v52
	v_cvt_pk_bf16_f32 v34, v34, v35
	v_cvt_pk_bf16_f32 v35, v36, v37
	v_lshlrev_b32_e32 v36, 16, v52
	v_and_b32_e32 v37, 0xffff0000, v40
	v_pk_mul_f32 v[42:43], v[60:61], v[42:43]
	v_lshlrev_b32_e32 v40, 16, v41
	v_pk_fma_f32 v[36:37], v[60:61], v[36:37], v[42:43] op_sel:[1,0,0] op_sel_hi:[0,1,1]
	v_and_b32_e32 v43, 0xffff0000, v41
	v_and_b32_e32 v41, 0xffff0000, v53
	v_lshlrev_b32_e32 v42, 16, v53
	v_pk_mul_f32 v[40:41], v[60:61], v[40:41]
	v_lshlrev_b32_e32 v48, 16, v44
	v_and_b32_e32 v49, 0xffff0000, v44
	v_pk_fma_f32 v[40:41], v[60:61], v[42:43], v[40:41] op_sel:[1,0,0] op_sel_hi:[0,1,1]
	v_lshlrev_b32_e32 v42, 16, v45
	v_and_b32_e32 v43, 0xffff0000, v45
	v_pk_fma_f32 v[36:37], v[38:39], v[48:49], v[36:37] op_sel_hi:[0,1,1]
	v_pk_fma_f32 v[42:43], v[38:39], v[42:43], v[40:41] op_sel_hi:[0,1,1]
	ds_read_b128 v[38:41], v88
	v_cvt_pk_bf16_f32 v36, v36, v37
	v_cvt_pk_bf16_f32 v37, v42, v43
	v_lshlrev_b64 v[42:43], 11, v[70:71]
	v_lshl_add_u64 v[48:49], v[58:59], 0, v[42:43]
	ds_read_b128 v[42:45], v89
	s_waitcnt vmcnt(4)
	v_lshlrev_b32_e32 v52, 16, v10
	s_waitcnt lgkmcnt(1)
	v_and_b32_e32 v53, 0xffff0000, v38
	v_lshlrev_b32_e32 v50, 16, v38
	v_and_b32_e32 v51, 0xffff0000, v10
	s_waitcnt vmcnt(3)
	v_lshlrev_b32_e32 v54, 16, v14
	v_and_b32_e32 v55, 0xffff0000, v14
	v_mov_b32_e32 v14, v24
	v_pk_mul_f32 v[24:25], v[22:23], v[52:53]
	v_lshlrev_b32_e32 v38, 16, v11
	v_pk_fma_f32 v[24:25], v[22:23], v[50:51], v[24:25] op_sel:[1,0,0] op_sel_hi:[0,1,1]
	v_pk_fma_f32 v[24:25], v[14:15], v[54:55], v[24:25] op_sel_hi:[0,1,1]
	v_cvt_pk_bf16_f32 v10, v24, v25
	v_lshlrev_b32_e32 v24, 16, v39
	v_and_b32_e32 v39, 0xffff0000, v39
	v_and_b32_e32 v25, 0xffff0000, v11
	v_pk_mul_f32 v[38:39], v[22:23], v[38:39]
	v_lshlrev_b32_e32 v50, 16, v15
	v_and_b32_e32 v51, 0xffff0000, v15
	v_pk_fma_f32 v[24:25], v[22:23], v[24:25], v[38:39] op_sel:[1,0,0] op_sel_hi:[0,1,1]
	v_pk_fma_f32 v[24:25], v[14:15], v[50:51], v[24:25] op_sel_hi:[0,1,1]
	v_lshlrev_b32_e32 v38, 16, v12
	v_and_b32_e32 v39, 0xffff0000, v40
	v_cvt_pk_bf16_f32 v11, v24, v25
	v_lshlrev_b32_e32 v24, 16, v40
	v_and_b32_e32 v25, 0xffff0000, v12
	v_pk_mul_f32 v[38:39], v[22:23], v[38:39]
	v_lshlrev_b32_e32 v50, 16, v16
	v_and_b32_e32 v51, 0xffff0000, v16
	v_pk_fma_f32 v[24:25], v[22:23], v[24:25], v[38:39] op_sel:[1,0,0] op_sel_hi:[0,1,1]
	v_pk_fma_f32 v[24:25], v[14:15], v[50:51], v[24:25] op_sel_hi:[0,1,1]
	v_lshlrev_b32_e32 v38, 16, v13
	v_and_b32_e32 v39, 0xffff0000, v41
	v_cvt_pk_bf16_f32 v12, v24, v25
	v_lshlrev_b32_e32 v24, 16, v41
	v_and_b32_e32 v25, 0xffff0000, v13
	v_pk_mul_f32 v[38:39], v[22:23], v[38:39]
	v_lshlrev_b32_e32 v16, 16, v17
	v_pk_fma_f32 v[22:23], v[22:23], v[24:25], v[38:39] op_sel:[1,0,0] op_sel_hi:[0,1,1]
	v_and_b32_e32 v17, 0xffff0000, v17
	v_pk_fma_f32 v[14:15], v[14:15], v[16:17], v[22:23] op_sel_hi:[0,1,1]
	v_cvt_pk_bf16_f32 v13, v14, v15
	v_lshlrev_b64 v[14:15], 11, v[28:29]
	v_lshl_add_u64 v[14:15], v[58:59], 0, v[14:15]
	global_store_dwordx4 v[46:47], v[30:33], off nt
	global_store_dwordx4 v[48:49], v[34:37], off nt
	global_store_dwordx4 v[14:15], v[10:13], off nt
	s_waitcnt vmcnt(3)
	v_lshlrev_b32_e32 v14, 16, v2
	v_and_b32_e32 v15, 0xffff0000, v2
	v_lshlrev_b32_e32 v12, 16, v6
	s_waitcnt lgkmcnt(0)
	v_and_b32_e32 v13, 0xffff0000, v42
	v_lshlrev_b32_e32 v10, 16, v42
	v_and_b32_e32 v11, 0xffff0000, v6
	v_pk_mul_f32 v[12:13], v[18:19], v[12:13]
	v_mov_b32_e32 v6, v20
	v_pk_fma_f32 v[10:11], v[18:19], v[10:11], v[12:13] op_sel:[1,0,0] op_sel_hi:[0,1,1]
	v_pk_fma_f32 v[10:11], v[6:7], v[14:15], v[10:11] op_sel_hi:[0,1,1]
	v_lshlrev_b32_e32 v12, 16, v7
	v_and_b32_e32 v13, 0xffff0000, v43
	v_cvt_pk_bf16_f32 v2, v10, v11
	v_lshlrev_b32_e32 v10, 16, v43
	v_and_b32_e32 v11, 0xffff0000, v7
	v_pk_mul_f32 v[12:13], v[18:19], v[12:13]
	v_lshlrev_b32_e32 v14, 16, v3
	v_and_b32_e32 v15, 0xffff0000, v3
	v_pk_fma_f32 v[10:11], v[18:19], v[10:11], v[12:13] op_sel:[1,0,0] op_sel_hi:[0,1,1]
	v_pk_fma_f32 v[10:11], v[6:7], v[14:15], v[10:11] op_sel_hi:[0,1,1]
	v_lshlrev_b32_e32 v12, 16, v8
	v_and_b32_e32 v13, 0xffff0000, v44
	v_cvt_pk_bf16_f32 v3, v10, v11
	v_lshlrev_b32_e32 v10, 16, v44
	v_and_b32_e32 v11, 0xffff0000, v8
	v_pk_mul_f32 v[12:13], v[18:19], v[12:13]
	v_lshlrev_b32_e32 v14, 16, v4
	v_and_b32_e32 v15, 0xffff0000, v4
	v_pk_fma_f32 v[10:11], v[18:19], v[10:11], v[12:13] op_sel:[1,0,0] op_sel_hi:[0,1,1]
	v_pk_fma_f32 v[10:11], v[6:7], v[14:15], v[10:11] op_sel_hi:[0,1,1]
	v_cvt_pk_bf16_f32 v4, v10, v11
	v_and_b32_e32 v11, 0xffff0000, v9
	v_lshlrev_b32_e32 v8, 16, v9
	v_and_b32_e32 v9, 0xffff0000, v45
	v_lshlrev_b32_e32 v10, 16, v45
	v_pk_mul_f32 v[8:9], v[18:19], v[8:9]
	s_nop 0
	v_pk_fma_f32 v[8:9], v[18:19], v[10:11], v[8:9] op_sel:[1,0,0] op_sel_hi:[0,1,1]
	v_lshlrev_b32_e32 v10, 16, v5
	v_and_b32_e32 v11, 0xffff0000, v5
	v_pk_fma_f32 v[6:7], v[6:7], v[10:11], v[8:9] op_sel_hi:[0,1,1]
	v_cvt_pk_bf16_f32 v5, v6, v7
	v_lshlrev_b64 v[6:7], 11, v[26:27]
	v_lshl_add_u64 v[6:7], v[58:59], 0, v[6:7]
	global_store_dwordx4 v[6:7], v[2:5], off nt
	s_waitcnt lgkmcnt(0)

.LBB0_682:
	s_waitcnt vmcnt(0)
	v_mov_b32_e32 v66, v181
	s_nop 1
	v_permlane32_swap_b32_e32 v181, v66
	s_barrier
	s_and_saveexec_b64 s[10:11], s[2:3]
	v_add_f32_e32 v66, v181, v66
	ds_write_b32 v174, v66 offset:128
	s_or_b64 exec, exec, s[10:11]
	s_waitcnt lgkmcnt(0)
	ds_read_b128 v[72:75], v165 offset:128
	ds_read_b128 v[76:79], v165 offset:160
	s_lshl_b32 s10, s41, 12
	s_add_i32 s12, s10, 0
	s_add_i32 s12, s12, 0x10c00
	s_waitcnt lgkmcnt(1)
	v_rcp_f32_e32 v71, v72
	v_cmp_lt_f32_e32 vcc, 0, v72
	v_lshl_add_u32 v83, v177, 1, s12
	s_lshl_b64 s[8:9], s[8:9], 11
	v_cndmask_b32_e32 v72, 0, v71, vcc
	v_mul_f32_e32 v50, v50, v72
	v_bfe_u32 v71, v50, 16, 1
	v_add3_u32 v50, v50, v71, s40
	v_lshlrev_b32_e32 v71, 9, v176
	v_mul_f32_e32 v34, v34, v72
	v_rcp_f32_e32 v72, v73
	v_add_u32_e32 v71, v83, v71
	ds_write_b16_d16_hi v71, v50
	v_bfe_u32 v50, v34, 16, 1
	v_add3_u32 v34, v34, v50, s40
	v_cmp_lt_f32_e32 vcc, 0, v73
	ds_write_b16_d16_hi v71, v34 offset:64
	s_add_u32 s11, s8, s42
	v_cndmask_b32_e32 v34, 0, v72, vcc
	v_mul_f32_e32 v50, v51, v34
	v_bfe_u32 v51, v50, 16, 1
	v_add3_u32 v50, v50, v51, s40
	v_lshlrev_b32_e32 v51, 7, v179
	v_or_b32_e32 v72, 0x80, v51
	v_add_u32_e32 v72, v83, v72
	ds_write_b16_d16_hi v72, v50
	v_rcp_f32_e32 v50, v74
	v_mul_f32_e32 v34, v35, v34
	v_bfe_u32 v35, v34, 16, 1
	v_add3_u32 v34, v34, v35, s40
	v_cmp_lt_f32_e32 vcc, 0, v74
	ds_write_b16_d16_hi v72, v34 offset:64
	s_mul_i32 s8, s33, 3
	v_cndmask_b32_e32 v34, 0, v50, vcc
	v_mul_f32_e32 v35, v52, v34
	v_bfe_u32 v50, v35, 16, 1
	v_add3_u32 v35, v35, v50, s40
	v_or_b32_e32 v50, 0x100, v51
	v_mul_f32_e32 v34, v36, v34
	v_rcp_f32_e32 v36, v75
	v_add_u32_e32 v73, v83, v50
	ds_write_b16_d16_hi v73, v35
	v_bfe_u32 v35, v34, 16, 1
	v_add3_u32 v34, v34, v35, s40
	v_cmp_lt_f32_e32 vcc, 0, v75
	ds_write_b16_d16_hi v73, v34 offset:64
	s_addc_u32 s10, s9, 0
	v_cndmask_b32_e32 v34, 0, v36, vcc
	v_mul_f32_e32 v35, v53, v34
	v_bfe_u32 v36, v35, 16, 1
	v_add3_u32 v35, v35, v36, s40
	v_or_b32_e32 v36, 0x180, v51
	v_add_u32_e32 v53, v83, v36
	s_waitcnt lgkmcnt(6)
	v_rcp_f32_e32 v36, v76
	v_mul_f32_e32 v34, v37, v34
	ds_write_b16_d16_hi v53, v35
	v_bfe_u32 v35, v34, 16, 1
	v_add3_u32 v34, v34, v35, s40
	v_cmp_lt_f32_e32 vcc, 0, v76
	ds_write_b16_d16_hi v53, v34 offset:64
	s_ashr_i32 s9, s8, 31
	v_cndmask_b32_e32 v34, 0, v36, vcc
	v_mul_f32_e32 v35, v54, v34
	v_bfe_u32 v36, v35, 16, 1
	v_add3_u32 v35, v35, v36, s40
	v_or_b32_e32 v36, 0x400, v51
	v_add_u32_e32 v74, v83, v36
	v_rcp_f32_e32 v36, v77
	v_mul_f32_e32 v34, v38, v34
	ds_write_b16_d16_hi v74, v35
	v_bfe_u32 v35, v34, 16, 1
	v_add3_u32 v34, v34, v35, s40
	v_cmp_lt_f32_e32 vcc, 0, v77
	ds_write_b16_d16_hi v74, v34 offset:64
	s_lshl_b64 s[8:9], s[8:9], 2
	v_cndmask_b32_e32 v34, 0, v36, vcc
	v_mul_f32_e32 v35, v55, v34
	v_bfe_u32 v36, v35, 16, 1
	v_add3_u32 v35, v35, v36, s40
	v_or_b32_e32 v36, 0x480, v51
	v_add_u32_e32 v75, v83, v36
	v_rcp_f32_e32 v36, v78
	v_mul_f32_e32 v34, v39, v34
	ds_write_b16_d16_hi v75, v35
	v_bfe_u32 v35, v34, 16, 1
	v_add3_u32 v34, v34, v35, s40
	v_cmp_lt_f32_e32 vcc, 0, v78
	ds_write_b16_d16_hi v75, v34 offset:64
	s_add_u32 s8, s24, s8
	v_cndmask_b32_e32 v34, 0, v36, vcc
	v_mul_f32_e32 v35, v56, v34
	v_bfe_u32 v36, v35, 16, 1
	v_add3_u32 v35, v35, v36, s40
	v_or_b32_e32 v36, 0x500, v51
	v_add_u32_e32 v76, v83, v36
	v_rcp_f32_e32 v36, v79
	v_mul_f32_e32 v34, v40, v34
	ds_write_b16_d16_hi v76, v35
	v_bfe_u32 v35, v34, 16, 1
	v_cmp_lt_f32_e32 vcc, 0, v79
	v_add3_u32 v34, v34, v35, s40
	ds_write_b16_d16_hi v76, v34 offset:64
	v_cndmask_b32_e32 v38, 0, v36, vcc
	v_mul_f32_e32 v34, v57, v38
	v_bfe_u32 v35, v34, 16, 1
	v_add3_u32 v39, v34, v35, s40
	v_or_b32_e32 v34, 0x580, v51
	v_add_u32_e32 v57, v83, v34
	ds_read_b128 v[34:37], v165 offset:192
	ds_write_b16_d16_hi v57, v39
	v_mul_f32_e32 v50, v41, v38
	ds_read_b128 v[38:41], v165 offset:224
	v_bfe_u32 v52, v50, 16, 1
	s_waitcnt lgkmcnt(2)
	v_rcp_f32_e32 v54, v34
	v_cmp_lt_f32_e32 vcc, 0, v34
	v_add3_u32 v50, v50, v52, s40
	ds_write_b16_d16_hi v57, v50 offset:64
	v_cndmask_b32_e32 v34, 0, v54, vcc
	v_mul_f32_e32 v50, v58, v34
	v_bfe_u32 v52, v50, 16, 1
	v_add3_u32 v50, v50, v52, s40
	v_or_b32_e32 v52, 0x800, v51
	v_add_u32_e32 v77, v83, v52
	ds_write_b16_d16_hi v77, v50
	v_rcp_f32_e32 v50, v35
	v_mul_f32_e32 v34, v42, v34
	v_bfe_u32 v42, v34, 16, 1
	v_add3_u32 v34, v34, v42, s40
	v_cmp_lt_f32_e32 vcc, 0, v35
	ds_write_b16_d16_hi v77, v34 offset:64
	s_addc_u32 s9, s25, s9
	v_cndmask_b32_e32 v34, 0, v50, vcc
	v_mul_f32_e32 v35, v59, v34
	v_bfe_u32 v42, v35, 16, 1
	v_add3_u32 v35, v35, v42, s40
	v_or_b32_e32 v42, 0x880, v51
	v_add_u32_e32 v78, v83, v42
	v_rcp_f32_e32 v42, v36
	v_mul_f32_e32 v34, v43, v34
	ds_write_b16_d16_hi v78, v35
	v_bfe_u32 v35, v34, 16, 1
	v_add3_u32 v34, v34, v35, s40
	v_cmp_lt_f32_e32 vcc, 0, v36
	ds_write_b16_d16_hi v78, v34 offset:64
	s_add_u32 s42, s26, s6
	v_cndmask_b32_e32 v34, 0, v42, vcc
	v_mul_f32_e32 v35, v60, v34
	v_bfe_u32 v36, v35, 16, 1
	v_add3_u32 v35, v35, v36, s40
	v_or_b32_e32 v36, 0x900, v51
	v_add_u32_e32 v79, v83, v36
	v_rcp_f32_e32 v36, v37
	v_mul_f32_e32 v34, v44, v34
	ds_write_b16_d16_hi v79, v35
	v_bfe_u32 v35, v34, 16, 1
	v_add3_u32 v34, v34, v35, s40
	v_cmp_lt_f32_e32 vcc, 0, v37
	ds_write_b16_d16_hi v79, v34 offset:64
	v_lshlrev_b32_e32 v66, 1, v178
	v_cndmask_b32_e32 v34, 0, v36, vcc
	v_mul_f32_e32 v35, v61, v34
	v_bfe_u32 v36, v35, 16, 1
	v_add3_u32 v35, v35, v36, s40
	v_or_b32_e32 v36, 0x980, v51
	v_add_u32_e32 v80, v83, v36
	s_waitcnt lgkmcnt(7)
	v_rcp_f32_e32 v36, v38
	v_mul_f32_e32 v34, v45, v34
	ds_write_b16_d16_hi v80, v35
	v_bfe_u32 v35, v34, 16, 1
	v_add3_u32 v34, v34, v35, s40
	v_cmp_lt_f32_e32 vcc, 0, v38
	ds_write_b16_d16_hi v80, v34 offset:64
	s_addc_u32 s43, s27, s7
	v_cndmask_b32_e32 v34, 0, v36, vcc
	v_mul_f32_e32 v35, v62, v34
	v_bfe_u32 v36, v35, 16, 1
	v_add3_u32 v35, v35, v36, s40
	v_or_b32_e32 v36, 0xc00, v51
	v_add_u32_e32 v81, v83, v36
	v_rcp_f32_e32 v36, v39
	v_mul_f32_e32 v34, v46, v34
	ds_write_b16_d16_hi v81, v35
	v_bfe_u32 v35, v34, 16, 1
	v_add3_u32 v34, v34, v35, s40
	v_cmp_lt_f32_e32 vcc, 0, v39
	ds_write_b16_d16_hi v81, v34 offset:64
	v_and_b32_e32 v162, 0x70, v66
	v_cndmask_b32_e32 v34, 0, v36, vcc
	v_mul_f32_e32 v35, v63, v34
	v_bfe_u32 v36, v35, 16, 1
	v_add3_u32 v35, v35, v36, s40
	v_or_b32_e32 v36, 0xc80, v51
	v_add_u32_e32 v82, v83, v36
	v_rcp_f32_e32 v36, v40
	v_mul_f32_e32 v34, v47, v34
	ds_write_b16_d16_hi v82, v35
	v_bfe_u32 v35, v34, 16, 1
	v_add3_u32 v34, v34, v35, s40
	v_cmp_lt_f32_e32 vcc, 0, v40
	ds_write_b16_d16_hi v82, v34 offset:64
	v_lshrrev_b32_e32 v70, 3, v180
	v_cndmask_b32_e32 v34, 0, v36, vcc
	v_mul_f32_e32 v35, v64, v34
	v_bfe_u32 v36, v35, 16, 1
	v_add3_u32 v35, v35, v36, s40
	v_or_b32_e32 v36, 0xd00, v51
	v_add_u32_e32 v64, v83, v36
	v_rcp_f32_e32 v36, v41
	v_mul_f32_e32 v34, v48, v34
	ds_write_b16_d16_hi v64, v35
	v_bfe_u32 v35, v34, 16, 1
	v_add3_u32 v34, v34, v35, s40
	v_cmp_lt_f32_e32 vcc, 0, v41
	ds_write_b16_d16_hi v64, v34 offset:64
	v_lshl_add_u64 v[66:67], s[42:43], 0, v[162:163]
	v_cndmask_b32_e32 v34, 0, v36, vcc
	v_mul_f32_e32 v35, v65, v34
	v_bfe_u32 v36, v35, 16, 1
	v_add3_u32 v35, v35, v36, s40
	v_or_b32_e32 v36, 0xd80, v51
	v_add_u32_e32 v65, v83, v36
	v_mul_f32_e32 v34, v49, v34
	s_add_u32 s42, s28, s6
	ds_write_b16_d16_hi v65, v35
	v_bfe_u32 v35, v34, 16, 1
	s_addc_u32 s43, s29, s7
	v_add3_u32 v34, v34, v35, s40
	v_or_b32_e32 v120, s11, v70
	v_mov_b32_e32 v121, s10
	v_lshl_add_u64 v[68:69], s[42:43], 0, v[162:163]
	ds_write_b16_d16_hi v65, v34 offset:64
	v_lshlrev_b64 v[34:35], 10, v[120:121]
	s_waitcnt lgkmcnt(0)
	v_lshl_add_u64 v[36:37], v[66:67], 0, v[34:35]
	v_lshl_add_u64 v[34:35], v[68:69], 0, v[34:35]
	global_load_dwordx4 v[88:91], v[36:37], off
	global_load_dwordx4 v[92:95], v[34:35], off
	v_lshlrev_b64 v[36:37], 7, v[120:121]
	v_lshl_add_u64 v[34:35], s[8:9], 0, v[36:37]
	global_load_dwordx3 v[112:114], v[34:35], off
	v_or_b32_e32 v83, 8, v70
	v_or_b32_e32 v122, s11, v83
	v_mov_b32_e32 v123, s10
	v_lshlrev_b64 v[34:35], 10, v[122:123]
	v_lshl_add_u64 v[36:37], v[66:67], 0, v[34:35]
	v_lshl_add_u64 v[34:35], v[68:69], 0, v[34:35]
	global_load_dwordx4 v[96:99], v[36:37], off
	global_load_dwordx4 v[100:103], v[34:35], off
	v_lshlrev_b64 v[36:37], 7, v[122:123]
	v_lshl_add_u64 v[34:35], s[8:9], 0, v[36:37]
	global_load_dwordx3 v[116:118], v[34:35], off
	v_or_b32_e32 v84, 16, v70
	v_or_b32_e32 v62, s11, v84
	v_mov_b32_e32 v63, s10
	v_lshlrev_b64 v[34:35], 7, v[62:63]
	v_lshl_add_u64 v[34:35], s[8:9], 0, v[34:35]
	v_lshlrev_b64 v[36:37], 10, v[62:63]
	v_lshl_add_u64 v[38:39], v[66:67], 0, v[36:37]
	global_load_dwordx3 v[54:56], v[34:35], off
	global_load_dwordx4 v[42:45], v[38:39], off
	v_or_b32_e32 v85, 24, v70
	v_or_b32_e32 v60, s11, v85
	v_mov_b32_e32 v61, s10
	v_lshl_add_u64 v[34:35], v[68:69], 0, v[36:37]
	v_lshlrev_b64 v[36:37], 7, v[60:61]
	v_lshl_add_u64 v[36:37], s[8:9], 0, v[36:37]
	global_load_dwordx4 v[46:49], v[34:35], off
	global_load_dwordx3 v[50:52], v[36:37], off
	v_add_u32_e32 v119, s12, v162
	v_lshlrev_b64 v[34:35], 10, v[60:61]
	v_lshlrev_b32_e32 v38, 7, v70
	v_lshl_add_u64 v[36:37], v[66:67], 0, v[34:35]
	v_lshl_add_u64 v[34:35], v[68:69], 0, v[34:35]
	v_add_u32_e32 v86, v119, v38
	ds_read_b128 v[104:107], v86
	global_load_dwordx4 v[38:41], v[36:37], off
	s_nop 0
	global_load_dwordx4 v[34:37], v[34:35], off
	v_lshlrev_b32_e32 v87, 7, v83
	v_add_u32_e32 v87, v119, v87
	ds_read_b128 v[108:111], v87
	s_waitcnt lgkmcnt(1)
	v_and_b32_e32 v127, 0xffff0000, v104
	v_lshlrev_b32_e32 v124, 16, v104
	s_add_u32 s6, s30, s6
	s_addc_u32 s7, s31, s7
	v_lshl_add_u64 v[58:59], s[6:7], 0, v[162:163]
	s_waitcnt vmcnt(11)
	v_lshlrev_b32_e32 v126, 16, v88
	v_and_b32_e32 v125, 0xffff0000, v88
	s_waitcnt vmcnt(10)
	v_lshlrev_b32_e32 v128, 16, v92
	v_and_b32_e32 v129, 0xffff0000, v92
	s_waitcnt vmcnt(9)
	v_mov_b32_e32 v88, v114
	v_pk_mul_f32 v[114:115], v[112:113], v[126:127]
	v_lshlrev_b32_e32 v104, 16, v89
	v_pk_fma_f32 v[114:115], v[112:113], v[124:125], v[114:115] op_sel:[1,0,0] op_sel_hi:[0,1,1]
	v_pk_fma_f32 v[114:115], v[88:89], v[128:129], v[114:115] op_sel_hi:[0,1,1]
	v_cvt_pk_bf16_f32 v92, v114, v115
	v_lshlrev_b32_e32 v114, 16, v105
	v_and_b32_e32 v105, 0xffff0000, v105
	v_and_b32_e32 v115, 0xffff0000, v89
	v_pk_mul_f32 v[104:105], v[112:113], v[104:105]
	v_lshlrev_b32_e32 v124, 16, v93
	v_and_b32_e32 v125, 0xffff0000, v93
	v_pk_fma_f32 v[104:105], v[112:113], v[114:115], v[104:105] op_sel:[1,0,0] op_sel_hi:[0,1,1]
	v_pk_fma_f32 v[104:105], v[88:89], v[124:125], v[104:105] op_sel_hi:[0,1,1]
	v_lshlrev_b32_e32 v114, 16, v90
	v_and_b32_e32 v115, 0xffff0000, v106
	v_cvt_pk_bf16_f32 v93, v104, v105
	v_lshlrev_b32_e32 v104, 16, v106
	v_and_b32_e32 v105, 0xffff0000, v90
	v_pk_mul_f32 v[114:115], v[112:113], v[114:115]
	v_lshlrev_b32_e32 v124, 16, v94
	v_and_b32_e32 v125, 0xffff0000, v94
	v_pk_fma_f32 v[104:105], v[112:113], v[104:105], v[114:115] op_sel:[1,0,0] op_sel_hi:[0,1,1]
	v_pk_fma_f32 v[104:105], v[88:89], v[124:125], v[104:105] op_sel_hi:[0,1,1]
	v_cvt_pk_bf16_f32 v94, v104, v105
	v_and_b32_e32 v105, 0xffff0000, v91
	v_lshlrev_b32_e32 v90, 16, v91
	v_and_b32_e32 v91, 0xffff0000, v107
	v_lshlrev_b32_e32 v104, 16, v107
	v_pk_mul_f32 v[90:91], v[112:113], v[90:91]
	s_waitcnt vmcnt(7)
	v_lshlrev_b32_e32 v106, 16, v100
	v_pk_fma_f32 v[90:91], v[112:113], v[104:105], v[90:91] op_sel:[1,0,0] op_sel_hi:[0,1,1]
	v_lshlrev_b32_e32 v104, 16, v95
	v_and_b32_e32 v105, 0xffff0000, v95
	v_pk_fma_f32 v[88:89], v[88:89], v[104:105], v[90:91] op_sel_hi:[0,1,1]
	v_cvt_pk_bf16_f32 v95, v88, v89
	v_lshlrev_b64 v[88:89], 11, v[120:121]
	v_lshlrev_b32_e32 v104, 16, v96
	s_waitcnt lgkmcnt(0)
	v_and_b32_e32 v105, 0xffff0000, v108
	v_lshl_add_u64 v[90:91], v[58:59], 0, v[88:89]
	v_lshlrev_b32_e32 v88, 16, v108
	v_and_b32_e32 v89, 0xffff0000, v96
	s_waitcnt vmcnt(6)
	v_pk_mul_f32 v[104:105], v[116:117], v[104:105]
	v_and_b32_e32 v107, 0xffff0000, v100
	v_mov_b32_e32 v100, v118
	v_pk_fma_f32 v[88:89], v[116:117], v[88:89], v[104:105] op_sel:[1,0,0] op_sel_hi:[0,1,1]
	v_pk_fma_f32 v[88:89], v[100:101], v[106:107], v[88:89] op_sel_hi:[0,1,1]
	v_lshlrev_b32_e32 v104, 16, v97
	v_and_b32_e32 v105, 0xffff0000, v109
	v_cvt_pk_bf16_f32 v96, v88, v89
	v_lshlrev_b32_e32 v88, 16, v109
	v_and_b32_e32 v89, 0xffff0000, v97
	v_pk_mul_f32 v[104:105], v[116:117], v[104:105]
	v_lshlrev_b32_e32 v106, 16, v101
	v_and_b32_e32 v107, 0xffff0000, v101
	v_pk_fma_f32 v[88:89], v[116:117], v[88:89], v[104:105] op_sel:[1,0,0] op_sel_hi:[0,1,1]
	v_pk_fma_f32 v[88:89], v[100:101], v[106:107], v[88:89] op_sel_hi:[0,1,1]
	v_lshlrev_b32_e32 v104, 16, v98
	v_and_b32_e32 v105, 0xffff0000, v110
	v_cvt_pk_bf16_f32 v97, v88, v89
	v_lshlrev_b32_e32 v88, 16, v110
	v_and_b32_e32 v89, 0xffff0000, v98
	v_pk_mul_f32 v[104:105], v[116:117], v[104:105]
	v_lshlrev_b32_e32 v106, 16, v102
	v_and_b32_e32 v107, 0xffff0000, v102
	v_pk_fma_f32 v[88:89], v[116:117], v[88:89], v[104:105] op_sel:[1,0,0] op_sel_hi:[0,1,1]
	v_pk_fma_f32 v[88:89], v[100:101], v[106:107], v[88:89] op_sel_hi:[0,1,1]
	v_lshlrev_b32_e32 v104, 16, v99
	v_and_b32_e32 v105, 0xffff0000, v111
	v_cvt_pk_bf16_f32 v98, v88, v89
	v_lshlrev_b32_e32 v88, 16, v111
	v_and_b32_e32 v89, 0xffff0000, v99
	v_pk_mul_f32 v[104:105], v[116:117], v[104:105]
	v_lshlrev_b32_e32 v102, 16, v103
	v_pk_fma_f32 v[88:89], v[116:117], v[88:89], v[104:105] op_sel:[1,0,0] op_sel_hi:[0,1,1]
	v_and_b32_e32 v103, 0xffff0000, v103
	v_pk_fma_f32 v[88:89], v[100:101], v[102:103], v[88:89] op_sel_hi:[0,1,1]
	v_cvt_pk_bf16_f32 v99, v88, v89
	v_lshlrev_b32_e32 v88, 7, v84
	v_add_u32_e32 v88, v119, v88
	ds_read_b128 v[100:103], v88
	v_lshlrev_b32_e32 v89, 7, v85
	v_lshlrev_b64 v[104:105], 11, v[122:123]
	v_add_u32_e32 v89, v119, v89
	v_lshl_add_u64 v[108:109], v[58:59], 0, v[104:105]
	ds_read_b128 v[104:107], v89
	s_waitcnt vmcnt(4)
	v_lshlrev_b32_e32 v112, 16, v42
	s_waitcnt lgkmcnt(1)
	v_and_b32_e32 v113, 0xffff0000, v100
	v_lshlrev_b32_e32 v110, 16, v100
	v_and_b32_e32 v111, 0xffff0000, v42
	v_pk_mul_f32 v[112:113], v[54:55], v[112:113]
	s_waitcnt vmcnt(3)
	v_lshlrev_b32_e32 v114, 16, v46
	v_and_b32_e32 v115, 0xffff0000, v46
	v_mov_b32_e32 v46, v56
	v_pk_fma_f32 v[110:111], v[54:55], v[110:111], v[112:113] op_sel:[1,0,0] op_sel_hi:[0,1,1]
	v_pk_fma_f32 v[110:111], v[46:47], v[114:115], v[110:111] op_sel_hi:[0,1,1]
	v_cvt_pk_bf16_f32 v42, v110, v111
	v_lshlrev_b32_e32 v110, 16, v101
	v_lshlrev_b32_e32 v100, 16, v43
	v_and_b32_e32 v101, 0xffff0000, v101
	v_and_b32_e32 v111, 0xffff0000, v43
	v_pk_mul_f32 v[100:101], v[54:55], v[100:101]
	v_lshlrev_b32_e32 v112, 16, v47
	v_and_b32_e32 v113, 0xffff0000, v47
	v_pk_fma_f32 v[100:101], v[54:55], v[110:111], v[100:101] op_sel:[1,0,0] op_sel_hi:[0,1,1]
	v_pk_fma_f32 v[100:101], v[46:47], v[112:113], v[100:101] op_sel_hi:[0,1,1]
	v_lshlrev_b32_e32 v110, 16, v44
	v_and_b32_e32 v111, 0xffff0000, v102
	v_cvt_pk_bf16_f32 v43, v100, v101
	v_lshlrev_b32_e32 v100, 16, v102
	v_and_b32_e32 v101, 0xffff0000, v44
	v_pk_mul_f32 v[110:111], v[54:55], v[110:111]
	v_lshlrev_b32_e32 v112, 16, v48
	v_and_b32_e32 v113, 0xffff0000, v48
	v_pk_fma_f32 v[100:101], v[54:55], v[100:101], v[110:111] op_sel:[1,0,0] op_sel_hi:[0,1,1]
	v_pk_fma_f32 v[100:101], v[46:47], v[112:113], v[100:101] op_sel_hi:[0,1,1]
	v_cvt_pk_bf16_f32 v44, v100, v101
	v_lshlrev_b32_e32 v100, 16, v103
	v_lshlrev_b32_e32 v102, 16, v45
	v_and_b32_e32 v103, 0xffff0000, v103
	v_and_b32_e32 v101, 0xffff0000, v45
	v_pk_mul_f32 v[102:103], v[54:55], v[102:103]
	v_lshlrev_b32_e32 v48, 16, v49
	v_pk_fma_f32 v[54:55], v[54:55], v[100:101], v[102:103] op_sel:[1,0,0] op_sel_hi:[0,1,1]
	v_and_b32_e32 v49, 0xffff0000, v49
	v_pk_fma_f32 v[46:47], v[46:47], v[48:49], v[54:55] op_sel_hi:[0,1,1]
	v_cvt_pk_bf16_f32 v45, v46, v47
	v_lshlrev_b64 v[46:47], 11, v[62:63]
	v_lshl_add_u64 v[46:47], v[58:59], 0, v[46:47]
	global_store_dwordx4 v[90:91], v[92:95], off nt
	global_store_dwordx4 v[108:109], v[96:99], off nt
	global_store_dwordx4 v[46:47], v[42:45], off nt
	s_waitcnt vmcnt(3)
	v_lshlrev_b32_e32 v46, 16, v34
	v_and_b32_e32 v47, 0xffff0000, v34
	v_lshlrev_b32_e32 v44, 16, v38
	s_waitcnt lgkmcnt(0)
	v_and_b32_e32 v45, 0xffff0000, v104
	v_lshlrev_b32_e32 v42, 16, v104
	v_and_b32_e32 v43, 0xffff0000, v38
	v_pk_mul_f32 v[44:45], v[50:51], v[44:45]
	v_mov_b32_e32 v38, v52
	v_pk_fma_f32 v[42:43], v[50:51], v[42:43], v[44:45] op_sel:[1,0,0] op_sel_hi:[0,1,1]
	v_pk_fma_f32 v[42:43], v[38:39], v[46:47], v[42:43] op_sel_hi:[0,1,1]
	v_lshlrev_b32_e32 v44, 16, v39
	v_and_b32_e32 v45, 0xffff0000, v105
	v_cvt_pk_bf16_f32 v34, v42, v43
	v_lshlrev_b32_e32 v42, 16, v105
	v_and_b32_e32 v43, 0xffff0000, v39
	v_pk_mul_f32 v[44:45], v[50:51], v[44:45]
	v_lshlrev_b32_e32 v46, 16, v35
	v_and_b32_e32 v47, 0xffff0000, v35
	v_pk_fma_f32 v[42:43], v[50:51], v[42:43], v[44:45] op_sel:[1,0,0] op_sel_hi:[0,1,1]
	v_pk_fma_f32 v[42:43], v[38:39], v[46:47], v[42:43] op_sel_hi:[0,1,1]
	v_lshlrev_b32_e32 v44, 16, v40
	v_and_b32_e32 v45, 0xffff0000, v106
	v_cvt_pk_bf16_f32 v35, v42, v43
	v_lshlrev_b32_e32 v42, 16, v106
	v_and_b32_e32 v43, 0xffff0000, v40
	v_pk_mul_f32 v[44:45], v[50:51], v[44:45]
	v_lshlrev_b32_e32 v46, 16, v36
	v_and_b32_e32 v47, 0xffff0000, v36
	v_pk_fma_f32 v[42:43], v[50:51], v[42:43], v[44:45] op_sel:[1,0,0] op_sel_hi:[0,1,1]
	v_pk_fma_f32 v[42:43], v[38:39], v[46:47], v[42:43] op_sel_hi:[0,1,1]
	v_cvt_pk_bf16_f32 v36, v42, v43
	v_and_b32_e32 v43, 0xffff0000, v41
	v_lshlrev_b32_e32 v40, 16, v41
	v_and_b32_e32 v41, 0xffff0000, v107
	v_lshlrev_b32_e32 v42, 16, v107
	v_pk_mul_f32 v[40:41], v[50:51], v[40:41]
	s_nop 0
	v_pk_fma_f32 v[40:41], v[50:51], v[42:43], v[40:41] op_sel:[1,0,0] op_sel_hi:[0,1,1]
	v_lshlrev_b32_e32 v42, 16, v37
	v_and_b32_e32 v43, 0xffff0000, v37
	v_pk_fma_f32 v[38:39], v[38:39], v[42:43], v[40:41] op_sel_hi:[0,1,1]
	v_cvt_pk_bf16_f32 v37, v38, v39
	v_lshlrev_b64 v[38:39], 11, v[60:61]
	v_lshl_add_u64 v[38:39], v[58:59], 0, v[38:39]
	global_store_dwordx4 v[38:39], v[34:37], off nt
	s_waitcnt lgkmcnt(0)
	s_nop 1
	v_mov_b32_e32 v34, v175
	s_nop 1
	v_permlane32_swap_b32_e32 v175, v34
	s_and_saveexec_b64 s[6:7], s[2:3]
	s_cbranch_execz .LBB0_635
	v_add_f32_e32 v34, v175, v34
	ds_write_b32 v174, v34 offset:128
	s_branch .LBB0_635
